# GEMM K-loops: 36 provably redundant lgkmcnt waits between MFMAs removed
# speedup vs baseline: 1.0055x; 1.0055x over previous
; #define PG8_STAGE(bufoff, gbase, voff) do { const char* sb_ = (gbase); _Pragma("unroll") for (int _i = 0; _i < 2; ++_i) PG8_GLDS(sb_, (voff)[_i], bufoff, _i); } while (0)
; #define PG8_LDA(dst, b, h) do { if constexpr (F8) { _Pragma("unroll") for (int m = 0; m < 4; ++m) dst##8[m] = PG8_RD8(lds + PG8_SA(b, h) + aoff + m * 2048); } else { \
;         _Pragma("unroll") for (int m = 0; m < 4; ++m) _Pragma("unroll") for (int k = 0; k < 2; ++k) dst[m][k] = *(const PG8_LAS bf16x8*)(lds + PG8_SA(b, h) + aoff + m * 2048 + k * 1024); } } while (0)
; #define PG8_LDB(dst, b, h) do { if constexpr (F8) { _Pragma("unroll") for (int n = 0; n < 2; ++n) dst##8[n] = PG8_RD8(lds + PG8_SB(b, h) + boff + n * 2048); } else { \
;         _Pragma("unroll") for (int n = 0; n < 2; ++n) _Pragma("unroll") for (int k = 0; k < 2; ++k) dst[n][k] = *(const PG8_LAS bf16x8*)(lds + PG8_SB(b, h) + boff + n * 2048 + k * 1024); } } while (0)
; #define PG8_WAIT_V(n) asm volatile("s_waitcnt vmcnt(" #n ")" ::: "memory")
;     ...
;         for (int t = 0; t < nt; t += 2) {
;             const bool last = (t == nt - 2);
;             const size_t k1 = (size_t)(t + 1) * kstep;
;             const size_t k2 = last ? 0 : (size_t)(t + 2) * kstep, k3 = k2 + kstep;
;             const char* b2 = last ? nB : cB + (size_t)(t + 2) * kstep; const char* b3 = b2 + kstep;
;             PG8_LDB(B0, 0, 0); PG8_LDB(B1, 0, 1); PG8_SCHED; PG8_LDA(At, 0, 0); PG8_STAGE_A(PG8_SA(1, 1), 1, k1, false);
;             PG8_WAIT_V(8); PG8_WAIT_L(0); PG8_BAR; PG8_MMA(0, 0, At, B0); PG8_MMA(0, 1, At, B1); PG8_BAR; PG8_SCHED;
;             PG8_LDA(At, 0, 1); PG8_STAGE(PG8_SB(0, 0), b2, voffB); PG8_STAGE(PG8_SB(0, 1), b2 + hstep, voffB); PG8_STAGE_A(PG8_SA(0, 0), 0, k2, last);
;             PG8_WAIT_V(8); PG8_WAIT_L(0); PG8_BAR; PG8_MMA(1, 0, At, B0); PG8_MMA(1, 1, At, B1); PG8_BAR; PG8_SCHED;
;             PG8_LDB(B0, 1, 0); PG8_LDB(B1, 1, 1); PG8_SCHED; PG8_LDA(At, 1, 0); PG8_STAGE_A(PG8_SA(0, 1), 1, k2, last);
;             PG8_WAIT_V(8); PG8_WAIT_L(0); PG8_BAR; PG8_MMA(0, 0, At, B0); PG8_MMA(0, 1, At, B1); PG8_BAR; PG8_SCHED;
;             PG8_LDA(At, 1, 1); PG8_STAGE(PG8_SB(1, 0), b3, voffB); PG8_STAGE(PG8_SB(1, 1), b3 + hstep, voffB); PG8_STAGE_A(PG8_SA(1, 0), 0, k3, last);
;             PG8_WAIT_V(8); PG8_WAIT_L(0); PG8_BAR; PG8_MMA(1, 0, At, B0); PG8_MMA(1, 1, At, B1); PG8_BAR; PG8_SCHED;
;         }
.LBB4_306:
	ds_read_b128 v[128:131], v212
	ds_read_b128 v[132:135], v212 offset:16
	ds_read_b128 v[136:139], v212 offset:2048
	ds_read_b128 v[140:143], v212 offset:2064
	ds_read_b128 v[144:147], v213
	ds_read_b128 v[148:151], v213 offset:16
	ds_read_b128 v[152:155], v213 offset:2048
	ds_read_b128 v[156:159], v213 offset:2064
	s_add_i32 s21, s26, 0xfffc0080
	s_add_u32 s28, s8, s26
	s_addc_u32 s29, s9, s27
	s_add_u32 s28, s28, 0xfffc0080
	s_addc_u32 s29, s29, -1
	s_add_u32 s30, s6, s26
	s_addc_u32 s31, s7, s27
	s_cmp_eq_u32 s19, 12
	s_cselect_b32 s21, 0, s21
	s_cselect_b32 s29, s25, s29
	s_cselect_b32 s28, s24, s28
	ds_read_b128 v[160:163], v214
	ds_read_b128 v[164:167], v214 offset:16
	ds_read_b128 v[168:171], v214 offset:2048
	ds_read_b128 v[172:175], v214 offset:2064
	ds_read_b128 v[176:179], v214 offset:4096
	ds_read_b128 v[180:183], v214 offset:4112
	ds_read_b128 v[184:187], v214 offset:6144
	ds_read_b128 v[188:191], v214 offset:6160
	s_mov_b32 m0, s75
	s_nop 0
	global_load_lds_dwordx4 v208, s[30:31]
	s_nop 0
	s_mov_b32 m0, s76
	s_nop 0
	global_load_lds_dwordx4 v210, s[30:31]
	s_waitcnt vmcnt(8)
	s_waitcnt lgkmcnt(0)
	s_barrier
	s_setprio 1
	v_mfma_scale_f32_16x16x128_f8f6f4 v[120:123], v[128:135], v[160:167], v[120:123], v216, v215 op_sel_hi:[0,0,0]
	v_mfma_scale_f32_16x16x128_f8f6f4 v[124:127], v[136:143], v[160:167], v[124:127], v216, v215 op_sel_hi:[0,0,0]
	v_mfma_scale_f32_16x16x128_f8f6f4 v[104:107], v[128:135], v[168:175], v[104:107], v216, v215 op_sel_hi:[0,0,0]
	v_mfma_scale_f32_16x16x128_f8f6f4 v[108:111], v[136:143], v[168:175], v[108:111], v216, v215 op_sel_hi:[0,0,0]
	v_mfma_scale_f32_16x16x128_f8f6f4 v[198:201], v[128:135], v[176:183], v[88:91], v216, v215 op_sel_hi:[0,0,0]
	v_mfma_scale_f32_16x16x128_f8f6f4 v[202:205], v[136:143], v[176:183], v[92:95], v216, v215 op_sel_hi:[0,0,0]
	v_mfma_scale_f32_16x16x128_f8f6f4 v[232:235], v[128:135], v[184:191], v[72:75], v216, v215 op_sel_hi:[0,0,0]
	v_mfma_scale_f32_16x16x128_f8f6f4 v[236:239], v[136:143], v[184:191], v[76:79], v216, v215 op_sel_hi:[0,0,0]
	s_setprio 0
	s_setprio 1
	v_mfma_scale_f32_16x16x128_f8f6f4 v[112:115], v[144:151], v[160:167], v[112:115], v216, v215 op_sel_hi:[0,0,0]
	v_mfma_scale_f32_16x16x128_f8f6f4 v[116:119], v[152:159], v[160:167], v[116:119], v216, v215 op_sel_hi:[0,0,0]
	v_mfma_scale_f32_16x16x128_f8f6f4 v[96:99], v[144:151], v[168:175], v[96:99], v216, v215 op_sel_hi:[0,0,0]
	v_mfma_scale_f32_16x16x128_f8f6f4 v[100:103], v[152:159], v[168:175], v[100:103], v216, v215 op_sel_hi:[0,0,0]
	v_mfma_scale_f32_16x16x128_f8f6f4 v[160:163], v[144:151], v[176:183], v[80:83], v216, v215 op_sel_hi:[0,0,0]
	v_mfma_scale_f32_16x16x128_f8f6f4 v[164:167], v[152:159], v[176:183], v[84:87], v216, v215 op_sel_hi:[0,0,0]
	v_mfma_scale_f32_16x16x128_f8f6f4 v[168:171], v[144:151], v[184:191], v[64:67], v216, v215 op_sel_hi:[0,0,0]
	v_mfma_scale_f32_16x16x128_f8f6f4 v[172:175], v[152:159], v[184:191], v[68:71], v216, v215 op_sel_hi:[0,0,0]
	s_setprio 0
	s_barrier
	s_nop 3
	ds_read_b128 v[64:67], v214 offset:16384
	ds_read_b128 v[68:71], v214 offset:16400
	ds_read_b128 v[72:75], v214 offset:18432
	ds_read_b128 v[76:79], v214 offset:18448
	ds_read_b128 v[80:83], v214 offset:20480
	ds_read_b128 v[84:87], v214 offset:20496
	ds_read_b128 v[88:91], v214 offset:22528
	ds_read_b128 v[92:95], v214 offset:22544
	s_mov_b32 m0, s43
	s_nop 0
	global_load_lds_dwordx4 v209, s[28:29]
	s_cselect_b32 s78, s23, s7
	s_mov_b32 m0, s54
	s_nop 0
	global_load_lds_dwordx4 v211, s[28:29]
	s_cselect_b32 s79, s22, s6
	s_add_u32 s30, s28, 0x40000
	s_addc_u32 s31, s29, 0
	s_mov_b32 m0, s55
	s_nop 0
	global_load_lds_dwordx4 v209, s[30:31]
	s_nop 0
	s_mov_b32 m0, s56
	s_nop 0
	global_load_lds_dwordx4 v211, s[30:31]
	s_add_u32 s30, s79, s21
	s_addc_u32 s31, s78, 0
	s_mov_b32 m0, s42
	s_nop 0
	global_load_lds_dwordx4 v208, s[30:31]
	s_nop 0
	s_mov_b32 m0, s57
	s_nop 0
	global_load_lds_dwordx4 v210, s[30:31]
	s_waitcnt vmcnt(8)
	s_waitcnt lgkmcnt(0)
	s_barrier
	s_setprio 1
	v_mfma_scale_f32_16x16x128_f8f6f4 v[56:59], v[128:135], v[64:71], v[56:59], v216, v215 op_sel_hi:[0,0,0]
	v_mfma_scale_f32_16x16x128_f8f6f4 v[60:63], v[136:143], v[64:71], v[60:63], v216, v215 op_sel_hi:[0,0,0]
	v_mfma_scale_f32_16x16x128_f8f6f4 v[8:11], v[128:135], v[88:95], v[8:11], v216, v215 op_sel_hi:[0,0,0]
	v_mfma_scale_f32_16x16x128_f8f6f4 v[176:179], v[128:135], v[72:79], v[40:43], v216, v215 op_sel_hi:[0,0,0]
	v_mfma_scale_f32_16x16x128_f8f6f4 v[180:183], v[136:143], v[72:79], v[44:47], v216, v215 op_sel_hi:[0,0,0]
	v_mfma_scale_f32_16x16x128_f8f6f4 v[184:187], v[128:135], v[80:87], v[24:27], v216, v215 op_sel_hi:[0,0,0]
	v_mfma_scale_f32_16x16x128_f8f6f4 v[188:191], v[136:143], v[80:87], v[28:31], v216, v215 op_sel_hi:[0,0,0]
	v_mfma_scale_f32_16x16x128_f8f6f4 v[240:243], v[136:143], v[88:95], v[12:15], v216, v215 op_sel_hi:[0,0,0]
	s_setprio 0
	s_setprio 1
	v_mfma_scale_f32_16x16x128_f8f6f4 v[52:55], v[152:159], v[64:71], v[52:55], v216, v215 op_sel_hi:[0,0,0]
	v_mfma_scale_f32_16x16x128_f8f6f4 v[244:247], v[144:151], v[64:71], v[48:51], v216, v215 op_sel_hi:[0,0,0]
	v_mfma_scale_f32_16x16x128_f8f6f4 v[248:251], v[144:151], v[72:79], v[32:35], v216, v215 op_sel_hi:[0,0,0]
	v_mfma_scale_f32_16x16x128_f8f6f4 v[252:255], v[152:159], v[72:79], v[36:39], v216, v215 op_sel_hi:[0,0,0]
	v_mfma_scale_f32_16x16x128_f8f6f4 v[224:227], v[144:151], v[80:87], v[16:19], v216, v215 op_sel_hi:[0,0,0]
	v_mfma_scale_f32_16x16x128_f8f6f4 v[192:195], v[152:159], v[80:87], v[20:23], v216, v215 op_sel_hi:[0,0,0]
	v_mfma_scale_f32_16x16x128_f8f6f4 v[228:231], v[144:151], v[88:95], v[0:3], v216, v215 op_sel_hi:[0,0,0]
	v_mfma_scale_f32_16x16x128_f8f6f4 v[220:223], v[152:159], v[88:95], v[4:7], v216, v215 op_sel_hi:[0,0,0]
	s_setprio 0
	s_barrier
; #define PG8_STAGE(bufoff, gbase, voff) do { const char* sb_ = (gbase); _Pragma("unroll") for (int _i = 0; _i < 2; ++_i) PG8_GLDS(sb_, (voff)[_i], bufoff, _i); } while (0)
; #define PG8_LDA(dst, b, h) do { if constexpr (F8) { _Pragma("unroll") for (int m = 0; m < 4; ++m) dst##8[m] = PG8_RD8(lds + PG8_SA(b, h) + aoff + m * 2048); } else { \
;         _Pragma("unroll") for (int m = 0; m < 4; ++m) _Pragma("unroll") for (int k = 0; k < 2; ++k) dst[m][k] = *(const PG8_LAS bf16x8*)(lds + PG8_SA(b, h) + aoff + m * 2048 + k * 1024); } } while (0)
; #define PG8_LDB(dst, b, h) do { if constexpr (F8) { _Pragma("unroll") for (int n = 0; n < 2; ++n) dst##8[n] = PG8_RD8(lds + PG8_SB(b, h) + boff + n * 2048); } else { \
;         _Pragma("unroll") for (int n = 0; n < 2; ++n) _Pragma("unroll") for (int k = 0; k < 2; ++k) dst[n][k] = *(const PG8_LAS bf16x8*)(lds + PG8_SB(b, h) + boff + n * 2048 + k * 1024); } } while (0)
; #define PG8_WAIT_V(n) asm volatile("s_waitcnt vmcnt(" #n ")" ::: "memory")
;     ...
;         for (int t = 0; t < nt; t += 2) {
;             const bool last = (t == nt - 2);
;             const size_t k1 = (size_t)(t + 1) * kstep;
;             const size_t k2 = last ? 0 : (size_t)(t + 2) * kstep, k3 = k2 + kstep;
;             const char* b2 = last ? nB : cB + (size_t)(t + 2) * kstep; const char* b3 = b2 + kstep;
;             PG8_LDB(B0, 0, 0); PG8_LDB(B1, 0, 1); PG8_SCHED; PG8_LDA(At, 0, 0); PG8_STAGE_A(PG8_SA(1, 1), 1, k1, false);
;             PG8_WAIT_V(8); PG8_WAIT_L(0); PG8_BAR; PG8_MMA(0, 0, At, B0); PG8_MMA(0, 1, At, B1); PG8_BAR; PG8_SCHED;
;             PG8_LDA(At, 0, 1); PG8_STAGE(PG8_SB(0, 0), b2, voffB); PG8_STAGE(PG8_SB(0, 1), b2 + hstep, voffB); PG8_STAGE_A(PG8_SA(0, 0), 0, k2, last);
;             PG8_WAIT_V(8); PG8_WAIT_L(0); PG8_BAR; PG8_MMA(1, 0, At, B0); PG8_MMA(1, 1, At, B1); PG8_BAR; PG8_SCHED;
;             PG8_LDB(B0, 1, 0); PG8_LDB(B1, 1, 1); PG8_SCHED; PG8_LDA(At, 1, 0); PG8_STAGE_A(PG8_SA(0, 1), 1, k2, last);
;             PG8_WAIT_V(8); PG8_WAIT_L(0); PG8_BAR; PG8_MMA(0, 0, At, B0); PG8_MMA(0, 1, At, B1); PG8_BAR; PG8_SCHED;
;             PG8_LDA(At, 1, 1); PG8_STAGE(PG8_SB(1, 0), b3, voffB); PG8_STAGE(PG8_SB(1, 1), b3 + hstep, voffB); PG8_STAGE_A(PG8_SA(1, 0), 0, k3, last);
;             PG8_WAIT_V(8); PG8_WAIT_L(0); PG8_BAR; PG8_MMA(1, 0, At, B0); PG8_MMA(1, 1, At, B1); PG8_BAR; PG8_SCHED;
;         }
	s_nop 3
	ds_read_b128 v[0:3], v217
	ds_read_b128 v[4:7], v217 offset:16
	ds_read_b128 v[12:15], v217 offset:2048
	ds_read_b128 v[16:19], v217 offset:2064
	ds_read_b128 v[128:131], v218
	ds_read_b128 v[132:135], v218 offset:16
	ds_read_b128 v[136:139], v218 offset:2048
	ds_read_b128 v[140:143], v218 offset:2064
	ds_read_b128 v[20:23], v214 offset:32768
	ds_read_b128 v[24:27], v214 offset:32784
	ds_read_b128 v[28:31], v214 offset:34816
	ds_read_b128 v[32:35], v214 offset:34832
	ds_read_b128 v[36:39], v214 offset:36864
	ds_read_b128 v[40:43], v214 offset:36880
	ds_read_b128 v[44:47], v214 offset:38912
	ds_read_b128 v[48:51], v214 offset:38928
	s_add_u32 s78, s30, 0x40000
	s_addc_u32 s79, s31, 0
	s_mov_b32 m0, s58
	s_nop 0
	global_load_lds_dwordx4 v208, s[78:79]
	s_nop 0
	s_mov_b32 m0, s59
	s_nop 0
	global_load_lds_dwordx4 v210, s[78:79]
	s_waitcnt vmcnt(8)
	s_waitcnt lgkmcnt(0)
	s_barrier
	s_setprio 1
	v_mfma_scale_f32_16x16x128_f8f6f4 v[120:123], v[0:7], v[20:27], v[120:123], v216, v215 op_sel_hi:[0,0,0]
	v_mfma_scale_f32_16x16x128_f8f6f4 v[124:127], v[12:19], v[20:27], v[124:127], v216, v215 op_sel_hi:[0,0,0]
	v_mfma_scale_f32_16x16x128_f8f6f4 v[104:107], v[0:7], v[28:35], v[104:107], v216, v215 op_sel_hi:[0,0,0]
	v_mfma_scale_f32_16x16x128_f8f6f4 v[108:111], v[12:19], v[28:35], v[108:111], v216, v215 op_sel_hi:[0,0,0]
	v_mfma_scale_f32_16x16x128_f8f6f4 v[88:91], v[0:7], v[36:43], v[198:201], v216, v215 op_sel_hi:[0,0,0]
	v_mfma_scale_f32_16x16x128_f8f6f4 v[92:95], v[12:19], v[36:43], v[202:205], v216, v215 op_sel_hi:[0,0,0]
	v_mfma_scale_f32_16x16x128_f8f6f4 v[72:75], v[0:7], v[44:51], v[232:235], v216, v215 op_sel_hi:[0,0,0]
	v_mfma_scale_f32_16x16x128_f8f6f4 v[76:79], v[12:19], v[44:51], v[236:239], v216, v215 op_sel_hi:[0,0,0]
	s_setprio 0
	s_setprio 1
	v_mfma_scale_f32_16x16x128_f8f6f4 v[112:115], v[128:135], v[20:27], v[112:115], v216, v215 op_sel_hi:[0,0,0]
	v_mfma_scale_f32_16x16x128_f8f6f4 v[116:119], v[136:143], v[20:27], v[116:119], v216, v215 op_sel_hi:[0,0,0]
	v_mfma_scale_f32_16x16x128_f8f6f4 v[96:99], v[128:135], v[28:35], v[96:99], v216, v215 op_sel_hi:[0,0,0]
	v_mfma_scale_f32_16x16x128_f8f6f4 v[100:103], v[136:143], v[28:35], v[100:103], v216, v215 op_sel_hi:[0,0,0]
	v_mfma_scale_f32_16x16x128_f8f6f4 v[80:83], v[128:135], v[36:43], v[160:163], v216, v215 op_sel_hi:[0,0,0]
	v_mfma_scale_f32_16x16x128_f8f6f4 v[84:87], v[136:143], v[36:43], v[164:167], v216, v215 op_sel_hi:[0,0,0]
	v_mfma_scale_f32_16x16x128_f8f6f4 v[64:67], v[128:135], v[44:51], v[168:171], v216, v215 op_sel_hi:[0,0,0]
	v_mfma_scale_f32_16x16x128_f8f6f4 v[68:71], v[136:143], v[44:51], v[172:175], v216, v215 op_sel_hi:[0,0,0]
	s_setprio 0
	s_barrier
	ds_read_b128 v[32:35], v214 offset:49152
	ds_read_b128 v[36:39], v214 offset:49168
	ds_read_b128 v[144:147], v214 offset:51200
	ds_read_b128 v[148:151], v214 offset:51216
	ds_read_b128 v[152:155], v214 offset:53248
	ds_read_b128 v[156:159], v214 offset:53264
	ds_read_b128 v[160:163], v214 offset:55296
	ds_read_b128 v[164:167], v214 offset:55312
	s_add_u32 s78, s28, 0x80
	s_addc_u32 s79, s29, 0
	s_mov_b32 m0, s63
	s_nop 0
	global_load_lds_dwordx4 v209, s[78:79]
	s_add_u32 s28, s28, 0x40080
	s_mov_b32 m0, s64
	s_nop 0
	global_load_lds_dwordx4 v211, s[78:79]
	s_addc_u32 s29, s29, 0
	s_mov_b32 m0, s67
	s_nop 0
	global_load_lds_dwordx4 v209, s[28:29]
	s_nop 0
	s_mov_b32 m0, s74
	s_nop 0
	global_load_lds_dwordx4 v211, s[28:29]
	s_add_u32 s28, s30, 0x80
	s_addc_u32 s29, s31, 0
	s_mov_b32 m0, s65
	s_nop 0
	global_load_lds_dwordx4 v208, s[28:29]
	s_nop 0
	s_mov_b32 m0, s66
	s_nop 0
	global_load_lds_dwordx4 v210, s[28:29]
	s_waitcnt vmcnt(8)
	s_waitcnt lgkmcnt(0)
	s_barrier
	s_setprio 1
	v_mfma_scale_f32_16x16x128_f8f6f4 v[56:59], v[0:7], v[32:39], v[56:59], v216, v215 op_sel_hi:[0,0,0]
	v_mfma_scale_f32_16x16x128_f8f6f4 v[60:63], v[12:19], v[32:39], v[60:63], v216, v215 op_sel_hi:[0,0,0]
	v_mfma_scale_f32_16x16x128_f8f6f4 v[40:43], v[0:7], v[144:151], v[176:179], v216, v215 op_sel_hi:[0,0,0]
	v_mfma_scale_f32_16x16x128_f8f6f4 v[44:47], v[12:19], v[144:151], v[180:183], v216, v215 op_sel_hi:[0,0,0]
	v_mfma_scale_f32_16x16x128_f8f6f4 v[24:27], v[0:7], v[152:159], v[184:187], v216, v215 op_sel_hi:[0,0,0]
	v_mfma_scale_f32_16x16x128_f8f6f4 v[28:31], v[12:19], v[152:159], v[188:191], v216, v215 op_sel_hi:[0,0,0]
	v_mfma_scale_f32_16x16x128_f8f6f4 v[8:11], v[0:7], v[160:167], v[8:11], v216, v215 op_sel_hi:[0,0,0]
	v_mfma_scale_f32_16x16x128_f8f6f4 v[12:15], v[12:19], v[160:167], v[240:243], v216, v215 op_sel_hi:[0,0,0]
	s_setprio 0
	s_setprio 1
	v_mfma_scale_f32_16x16x128_f8f6f4 v[48:51], v[128:135], v[32:39], v[244:247], v216, v215 op_sel_hi:[0,0,0]
	v_mfma_scale_f32_16x16x128_f8f6f4 v[52:55], v[136:143], v[32:39], v[52:55], v216, v215 op_sel_hi:[0,0,0]
	v_mfma_scale_f32_16x16x128_f8f6f4 v[32:35], v[128:135], v[144:151], v[248:251], v216, v215 op_sel_hi:[0,0,0]
	v_mfma_scale_f32_16x16x128_f8f6f4 v[36:39], v[136:143], v[144:151], v[252:255], v216, v215 op_sel_hi:[0,0,0]
	v_mfma_scale_f32_16x16x128_f8f6f4 v[16:19], v[128:135], v[152:159], v[224:227], v216, v215 op_sel_hi:[0,0,0]
	v_mfma_scale_f32_16x16x128_f8f6f4 v[20:23], v[136:143], v[152:159], v[192:195], v216, v215 op_sel_hi:[0,0,0]
	v_mfma_scale_f32_16x16x128_f8f6f4 v[0:3], v[128:135], v[160:167], v[228:231], v216, v215 op_sel_hi:[0,0,0]
	v_mfma_scale_f32_16x16x128_f8f6f4 v[4:7], v[136:143], v[160:167], v[220:223], v216, v215 op_sel_hi:[0,0,0]
	s_setprio 0
	s_barrier
	s_add_i32 s19, s19, 2
	s_add_u32 s26, s26, 0x100
	s_addc_u32 s27, s27, 0
	s_cmp_gt_u32 s19, 13
	s_cbranch_scc0 .LBB4_306
	s_and_b64 vcc, exec, s[16:17]
	s_cbranch_vccz .LBB4_309
	s_barrier

; #define PG8_STAGE(bufoff, gbase, voff) do { const char* sb_ = (gbase); _Pragma("unroll") for (int _i = 0; _i < 2; ++_i) PG8_GLDS(sb_, (voff)[_i], bufoff, _i); } while (0)
; #define PG8_LDA(dst, b, h) do { if constexpr (F8) { _Pragma("unroll") for (int m = 0; m < 4; ++m) dst##8[m] = PG8_RD8(lds + PG8_SA(b, h) + aoff + m * 2048); } else { \
;         _Pragma("unroll") for (int m = 0; m < 4; ++m) _Pragma("unroll") for (int k = 0; k < 2; ++k) dst[m][k] = *(const PG8_LAS bf16x8*)(lds + PG8_SA(b, h) + aoff + m * 2048 + k * 1024); } } while (0)
; #define PG8_LDB(dst, b, h) do { if constexpr (F8) { _Pragma("unroll") for (int n = 0; n < 2; ++n) dst##8[n] = PG8_RD8(lds + PG8_SB(b, h) + boff + n * 2048); } else { \
;         _Pragma("unroll") for (int n = 0; n < 2; ++n) _Pragma("unroll") for (int k = 0; k < 2; ++k) dst[n][k] = *(const PG8_LAS bf16x8*)(lds + PG8_SB(b, h) + boff + n * 2048 + k * 1024); } } while (0)
; #define PG8_WAIT_V(n) asm volatile("s_waitcnt vmcnt(" #n ")" ::: "memory")
;     ...
;         for (int t = 0; t < nt; t += 2) {
;             const bool last = (t == nt - 2);
;             const size_t k1 = (size_t)(t + 1) * kstep;
;             const size_t k2 = last ? 0 : (size_t)(t + 2) * kstep, k3 = k2 + kstep;
;             const char* b2 = last ? nB : cB + (size_t)(t + 2) * kstep; const char* b3 = b2 + kstep;
;             PG8_LDB(B0, 0, 0); PG8_LDB(B1, 0, 1); PG8_SCHED; PG8_LDA(At, 0, 0); PG8_STAGE_A(PG8_SA(1, 1), 1, k1, false);
;             PG8_WAIT_V(8); PG8_WAIT_L(0); PG8_BAR; PG8_MMA(0, 0, At, B0); PG8_MMA(0, 1, At, B1); PG8_BAR; PG8_SCHED;
;             PG8_LDA(At, 0, 1); PG8_STAGE(PG8_SB(0, 0), b2, voffB); PG8_STAGE(PG8_SB(0, 1), b2 + hstep, voffB); PG8_STAGE_A(PG8_SA(0, 0), 0, k2, last);
;             PG8_WAIT_V(8); PG8_WAIT_L(0); PG8_BAR; PG8_MMA(1, 0, At, B0); PG8_MMA(1, 1, At, B1); PG8_BAR; PG8_SCHED;
;             PG8_LDB(B0, 1, 0); PG8_LDB(B1, 1, 1); PG8_SCHED; PG8_LDA(At, 1, 0); PG8_STAGE_A(PG8_SA(0, 1), 1, k2, last);
;             PG8_WAIT_V(8); PG8_WAIT_L(0); PG8_BAR; PG8_MMA(0, 0, At, B0); PG8_MMA(0, 1, At, B1); PG8_BAR; PG8_SCHED;
;             PG8_LDA(At, 1, 1); PG8_STAGE(PG8_SB(1, 0), b3, voffB); PG8_STAGE(PG8_SB(1, 1), b3 + hstep, voffB); PG8_STAGE_A(PG8_SA(1, 0), 0, k3, last);
;             PG8_WAIT_V(8); PG8_WAIT_L(0); PG8_BAR; PG8_MMA(1, 0, At, B0); PG8_MMA(1, 1, At, B1); PG8_BAR; PG8_SCHED;
;         }
.LBB4_1055:
	ds_read_b128 v[152:155], v149
	ds_read_b128 v[156:159], v149 offset:1024
	ds_read_b128 v[160:163], v149 offset:2048
	ds_read_b128 v[164:167], v149 offset:3072
	ds_read_b128 v[168:171], v150
	ds_read_b128 v[172:175], v150 offset:1024
	ds_read_b128 v[176:179], v150 offset:2048
	ds_read_b128 v[180:183], v150 offset:3072
	s_add_u32 s36, s34, 0x100
	s_addc_u32 s37, s35, 0
	s_add_u32 s80, s77, s34
	s_addc_u32 s81, s78, s35
	s_cmp_eq_u32 s79, 28
	s_cselect_b64 s[40:41], -1, 0
	s_and_b64 s[38:39], s[40:41], exec
	s_cselect_b32 s82, 0, s36
	s_cselect_b32 s39, s21, s81
	s_cselect_b32 s38, s23, s80
	v_lshl_add_u64 v[216:217], v[144:145], 0, s[34:35]
	s_add_i32 m0, s29, 0xc000
	ds_read_b128 v[184:187], v151
	ds_read_b128 v[188:191], v151 offset:1024
	ds_read_b128 v[192:195], v151 offset:2048
	ds_read_b128 v[196:199], v151 offset:3072
	ds_read_b128 v[200:203], v151 offset:4096
	ds_read_b128 v[204:207], v151 offset:5120
	ds_read_b128 v[208:211], v151 offset:6144
	ds_read_b128 v[212:215], v151 offset:7168
	global_load_lds_dwordx4 v[216:217], off
	v_lshl_add_u64 v[216:217], v[146:147], 0, s[34:35]
	s_add_i32 m0, s29, 0xe000
	s_nop 0
	global_load_lds_dwordx4 v[216:217], off
	s_waitcnt vmcnt(8)
	s_waitcnt lgkmcnt(0)
	s_barrier
	s_setprio 1
	v_mfma_f32_16x16x32_bf16 v[124:127], v[152:155], v[184:187], v[124:127]
	v_mfma_f32_16x16x32_bf16 v[120:123], v[160:163], v[184:187], v[120:123]
	v_mfma_f32_16x16x32_bf16 v[112:115], v[152:155], v[192:195], v[112:115]
	v_mfma_f32_16x16x32_bf16 v[104:107], v[160:163], v[192:195], v[104:107]
	v_mfma_f32_16x16x32_bf16 v[96:99], v[152:155], v[200:203], v[96:99]
	v_mfma_f32_16x16x32_bf16 v[88:91], v[160:163], v[200:203], v[88:91]
	v_mfma_f32_16x16x32_bf16 v[80:83], v[152:155], v[208:211], v[80:83]
	v_mfma_f32_16x16x32_bf16 v[72:75], v[160:163], v[208:211], v[72:75]
	v_mfma_f32_16x16x32_bf16 v[124:127], v[156:159], v[188:191], v[124:127]
	v_mfma_f32_16x16x32_bf16 v[120:123], v[164:167], v[188:191], v[120:123]
	v_mfma_f32_16x16x32_bf16 v[112:115], v[156:159], v[196:199], v[112:115]
	v_mfma_f32_16x16x32_bf16 v[104:107], v[164:167], v[196:199], v[104:107]
	v_mfma_f32_16x16x32_bf16 v[96:99], v[156:159], v[204:207], v[96:99]
	v_mfma_f32_16x16x32_bf16 v[88:91], v[164:167], v[204:207], v[88:91]
	v_mfma_f32_16x16x32_bf16 v[80:83], v[156:159], v[212:215], v[80:83]
	v_mfma_f32_16x16x32_bf16 v[72:75], v[164:167], v[212:215], v[72:75]
	s_setprio 0
	s_setprio 1
	v_mfma_f32_16x16x32_bf16 v[116:119], v[168:171], v[184:187], v[116:119]
	v_mfma_f32_16x16x32_bf16 v[108:111], v[176:179], v[184:187], v[108:111]
	v_mfma_f32_16x16x32_bf16 v[100:103], v[168:171], v[192:195], v[100:103]
	v_mfma_f32_16x16x32_bf16 v[92:95], v[176:179], v[192:195], v[92:95]
	v_mfma_f32_16x16x32_bf16 v[84:87], v[168:171], v[200:203], v[84:87]
	v_mfma_f32_16x16x32_bf16 v[76:79], v[176:179], v[200:203], v[76:79]
	v_mfma_f32_16x16x32_bf16 v[68:71], v[168:171], v[208:211], v[68:71]
	v_mfma_f32_16x16x32_bf16 v[64:67], v[176:179], v[208:211], v[64:67]
	v_mfma_f32_16x16x32_bf16 v[116:119], v[172:175], v[188:191], v[116:119]
	v_mfma_f32_16x16x32_bf16 v[108:111], v[180:183], v[188:191], v[108:111]
	v_mfma_f32_16x16x32_bf16 v[100:103], v[172:175], v[196:199], v[100:103]
	v_mfma_f32_16x16x32_bf16 v[92:95], v[180:183], v[196:199], v[92:95]
	v_mfma_f32_16x16x32_bf16 v[84:87], v[172:175], v[204:207], v[84:87]
	v_mfma_f32_16x16x32_bf16 v[76:79], v[180:183], v[204:207], v[76:79]
	v_mfma_f32_16x16x32_bf16 v[68:71], v[172:175], v[212:215], v[68:71]
	v_mfma_f32_16x16x32_bf16 v[64:67], v[180:183], v[212:215], v[64:67]
	s_setprio 0
	s_barrier
	s_add_i32 s34, s67, s57
	v_lshl_add_u64 v[216:217], s[38:39], 0, v[130:131]
	s_mov_b32 m0, s34
	ds_read_b128 v[184:187], v151 offset:16384
	ds_read_b128 v[188:191], v151 offset:17408
	ds_read_b128 v[192:195], v151 offset:18432
	ds_read_b128 v[196:199], v151 offset:19456
	ds_read_b128 v[200:203], v151 offset:20480
	ds_read_b128 v[204:207], v151 offset:21504
	ds_read_b128 v[208:211], v151 offset:22528
	ds_read_b128 v[212:215], v151 offset:23552
	global_load_lds_dwordx4 v[216:217], off
	s_add_i32 m0, s34, 0x2000
	s_add_u32 s34, s38, 0x80000
	v_lshl_add_u64 v[218:219], s[38:39], 0, v[134:135]
	s_addc_u32 s35, s39, 0
	s_add_i32 s80, s74, s57
	global_load_lds_dwordx4 v[218:219], off
	v_lshl_add_u64 v[220:221], s[34:35], 0, v[130:131]
	s_mov_b32 m0, s80
	s_nop 0
	global_load_lds_dwordx4 v[220:221], off
	v_lshl_add_u64 v[220:221], s[34:35], 0, v[134:135]
	s_add_i32 m0, s80, 0x2000
	s_and_b64 s[34:35], s[2:3], s[40:41]
	s_and_b64 s[34:35], s[34:35], exec
	s_cselect_b32 s34, s24, s30
	s_cselect_b32 s35, s25, s31
	s_add_u32 s34, s34, s82
	s_addc_u32 s35, s35, 0
	global_load_lds_dwordx4 v[220:221], off
	v_lshl_add_u64 v[220:221], s[34:35], 0, v[128:129]
	s_mov_b32 m0, s29
	v_lshl_add_u64 v[222:223], s[34:35], 0, v[132:133]
	global_load_lds_dwordx4 v[220:221], off
	s_mov_b32 m0, s58
	s_nop 0
	global_load_lds_dwordx4 v[222:223], off
	s_waitcnt vmcnt(8)
	s_waitcnt lgkmcnt(0)
	s_barrier
; #define PG8_STAGE(bufoff, gbase, voff) do { const char* sb_ = (gbase); _Pragma("unroll") for (int _i = 0; _i < 2; ++_i) PG8_GLDS(sb_, (voff)[_i], bufoff, _i); } while (0)
; #define PG8_LDA(dst, b, h) do { if constexpr (F8) { _Pragma("unroll") for (int m = 0; m < 4; ++m) dst##8[m] = PG8_RD8(lds + PG8_SA(b, h) + aoff + m * 2048); } else { \
;         _Pragma("unroll") for (int m = 0; m < 4; ++m) _Pragma("unroll") for (int k = 0; k < 2; ++k) dst[m][k] = *(const PG8_LAS bf16x8*)(lds + PG8_SA(b, h) + aoff + m * 2048 + k * 1024); } } while (0)
; #define PG8_LDB(dst, b, h) do { if constexpr (F8) { _Pragma("unroll") for (int n = 0; n < 2; ++n) dst##8[n] = PG8_RD8(lds + PG8_SB(b, h) + boff + n * 2048); } else { \
;         _Pragma("unroll") for (int n = 0; n < 2; ++n) _Pragma("unroll") for (int k = 0; k < 2; ++k) dst[n][k] = *(const PG8_LAS bf16x8*)(lds + PG8_SB(b, h) + boff + n * 2048 + k * 1024); } } while (0)
; #define PG8_WAIT_V(n) asm volatile("s_waitcnt vmcnt(" #n ")" ::: "memory")
;     ...
;         for (int t = 0; t < nt; t += 2) {
;             const bool last = (t == nt - 2);
;             const size_t k1 = (size_t)(t + 1) * kstep;
;             const size_t k2 = last ? 0 : (size_t)(t + 2) * kstep, k3 = k2 + kstep;
;             const char* b2 = last ? nB : cB + (size_t)(t + 2) * kstep; const char* b3 = b2 + kstep;
;             PG8_LDB(B0, 0, 0); PG8_LDB(B1, 0, 1); PG8_SCHED; PG8_LDA(At, 0, 0); PG8_STAGE_A(PG8_SA(1, 1), 1, k1, false);
;             PG8_WAIT_V(8); PG8_WAIT_L(0); PG8_BAR; PG8_MMA(0, 0, At, B0); PG8_MMA(0, 1, At, B1); PG8_BAR; PG8_SCHED;
;             PG8_LDA(At, 0, 1); PG8_STAGE(PG8_SB(0, 0), b2, voffB); PG8_STAGE(PG8_SB(0, 1), b2 + hstep, voffB); PG8_STAGE_A(PG8_SA(0, 0), 0, k2, last);
;             PG8_WAIT_V(8); PG8_WAIT_L(0); PG8_BAR; PG8_MMA(1, 0, At, B0); PG8_MMA(1, 1, At, B1); PG8_BAR; PG8_SCHED;
;             PG8_LDB(B0, 1, 0); PG8_LDB(B1, 1, 1); PG8_SCHED; PG8_LDA(At, 1, 0); PG8_STAGE_A(PG8_SA(0, 1), 1, k2, last);
;             PG8_WAIT_V(8); PG8_WAIT_L(0); PG8_BAR; PG8_MMA(0, 0, At, B0); PG8_MMA(0, 1, At, B1); PG8_BAR; PG8_SCHED;
;             PG8_LDA(At, 1, 1); PG8_STAGE(PG8_SB(1, 0), b3, voffB); PG8_STAGE(PG8_SB(1, 1), b3 + hstep, voffB); PG8_STAGE_A(PG8_SA(1, 0), 0, k3, last);
;             PG8_WAIT_V(8); PG8_WAIT_L(0); PG8_BAR; PG8_MMA(1, 0, At, B0); PG8_MMA(1, 1, At, B1); PG8_BAR; PG8_SCHED;
;         }
	s_setprio 1
	v_mfma_f32_16x16x32_bf16 v[60:63], v[152:155], v[184:187], v[60:63]
	v_mfma_f32_16x16x32_bf16 v[56:59], v[160:163], v[184:187], v[56:59]
	v_mfma_f32_16x16x32_bf16 v[52:55], v[152:155], v[192:195], v[52:55]
	v_mfma_f32_16x16x32_bf16 v[44:47], v[160:163], v[192:195], v[44:47]
	v_mfma_f32_16x16x32_bf16 v[36:39], v[152:155], v[200:203], v[36:39]
	v_mfma_f32_16x16x32_bf16 v[28:31], v[160:163], v[200:203], v[28:31]
	v_mfma_f32_16x16x32_bf16 v[20:23], v[152:155], v[208:211], v[20:23]
	v_mfma_f32_16x16x32_bf16 v[12:15], v[160:163], v[208:211], v[12:15]
	v_mfma_f32_16x16x32_bf16 v[60:63], v[156:159], v[188:191], v[60:63]
	v_mfma_f32_16x16x32_bf16 v[56:59], v[164:167], v[188:191], v[56:59]
	v_mfma_f32_16x16x32_bf16 v[52:55], v[156:159], v[196:199], v[52:55]
	v_mfma_f32_16x16x32_bf16 v[44:47], v[164:167], v[196:199], v[44:47]
	v_mfma_f32_16x16x32_bf16 v[36:39], v[156:159], v[204:207], v[36:39]
	v_mfma_f32_16x16x32_bf16 v[28:31], v[164:167], v[204:207], v[28:31]
	v_mfma_f32_16x16x32_bf16 v[20:23], v[156:159], v[212:215], v[20:23]
	v_mfma_f32_16x16x32_bf16 v[12:15], v[164:167], v[212:215], v[12:15]
	s_setprio 0
	s_setprio 1
	v_mfma_f32_16x16x32_bf16 v[48:51], v[168:171], v[184:187], v[48:51]
	v_mfma_f32_16x16x32_bf16 v[40:43], v[176:179], v[184:187], v[40:43]
	v_mfma_f32_16x16x32_bf16 v[32:35], v[168:171], v[192:195], v[32:35]
	v_mfma_f32_16x16x32_bf16 v[24:27], v[176:179], v[192:195], v[24:27]
	v_mfma_f32_16x16x32_bf16 v[16:19], v[168:171], v[200:203], v[16:19]
	v_mfma_f32_16x16x32_bf16 v[8:11], v[176:179], v[200:203], v[8:11]
	v_mfma_f32_16x16x32_bf16 v[4:7], v[168:171], v[208:211], v[4:7]
	v_mfma_f32_16x16x32_bf16 v[0:3], v[176:179], v[208:211], v[0:3]
	v_mfma_f32_16x16x32_bf16 v[48:51], v[172:175], v[188:191], v[48:51]
	v_mfma_f32_16x16x32_bf16 v[40:43], v[180:183], v[188:191], v[40:43]
	v_mfma_f32_16x16x32_bf16 v[32:35], v[172:175], v[196:199], v[32:35]
	v_mfma_f32_16x16x32_bf16 v[24:27], v[180:183], v[196:199], v[24:27]
	v_mfma_f32_16x16x32_bf16 v[16:19], v[172:175], v[204:207], v[16:19]
	v_mfma_f32_16x16x32_bf16 v[8:11], v[180:183], v[204:207], v[8:11]
	v_mfma_f32_16x16x32_bf16 v[4:7], v[172:175], v[212:215], v[4:7]
	v_mfma_f32_16x16x32_bf16 v[0:3], v[180:183], v[212:215], v[0:3]
	s_setprio 0
	s_barrier
	s_add_i32 s40, 0, 0x18000
	s_add_i32 s41, 0, 0x1c000
	v_add_u32_e32 v164, s40, v148
	v_add_u32_e32 v180, s41, v148
	ds_read_b128 v[152:155], v164
	ds_read_b128 v[156:159], v164 offset:1024
	ds_read_b128 v[160:163], v164 offset:2048
	ds_read_b128 v[164:167], v164 offset:3072
	ds_read_b128 v[168:171], v180
	ds_read_b128 v[172:175], v180 offset:1024
	ds_read_b128 v[176:179], v180 offset:2048
	ds_read_b128 v[180:183], v180 offset:3072
	s_add_u32 s34, s34, 0x80000
	s_addc_u32 s35, s35, 0
	s_mov_b32 m0, s59
	v_lshl_add_u64 v[224:225], s[34:35], 0, v[128:129]
	ds_read_b128 v[184:187], v151 offset:32768
	ds_read_b128 v[188:191], v151 offset:33792
	ds_read_b128 v[192:195], v151 offset:34816
	ds_read_b128 v[196:199], v151 offset:35840
	ds_read_b128 v[200:203], v151 offset:36864
	ds_read_b128 v[204:207], v151 offset:37888
	ds_read_b128 v[208:211], v151 offset:38912
	ds_read_b128 v[212:215], v151 offset:39936
	global_load_lds_dwordx4 v[224:225], off
	v_lshl_add_u64 v[224:225], s[34:35], 0, v[132:133]
	s_mov_b32 m0, s60
	s_nop 0
	global_load_lds_dwordx4 v[224:225], off
	s_waitcnt vmcnt(8)
	s_waitcnt lgkmcnt(0)
	s_barrier
	s_setprio 1
	v_mfma_f32_16x16x32_bf16 v[124:127], v[152:155], v[184:187], v[124:127]
	v_mfma_f32_16x16x32_bf16 v[120:123], v[160:163], v[184:187], v[120:123]
	v_mfma_f32_16x16x32_bf16 v[112:115], v[152:155], v[192:195], v[112:115]
	v_mfma_f32_16x16x32_bf16 v[104:107], v[160:163], v[192:195], v[104:107]
	v_mfma_f32_16x16x32_bf16 v[96:99], v[152:155], v[200:203], v[96:99]
	v_mfma_f32_16x16x32_bf16 v[88:91], v[160:163], v[200:203], v[88:91]
	v_mfma_f32_16x16x32_bf16 v[80:83], v[152:155], v[208:211], v[80:83]
	v_mfma_f32_16x16x32_bf16 v[72:75], v[160:163], v[208:211], v[72:75]
	v_mfma_f32_16x16x32_bf16 v[124:127], v[156:159], v[188:191], v[124:127]
	v_mfma_f32_16x16x32_bf16 v[120:123], v[164:167], v[188:191], v[120:123]
	v_mfma_f32_16x16x32_bf16 v[112:115], v[156:159], v[196:199], v[112:115]
	v_mfma_f32_16x16x32_bf16 v[104:107], v[164:167], v[196:199], v[104:107]
	v_mfma_f32_16x16x32_bf16 v[96:99], v[156:159], v[204:207], v[96:99]
	v_mfma_f32_16x16x32_bf16 v[88:91], v[164:167], v[204:207], v[88:91]
	v_mfma_f32_16x16x32_bf16 v[80:83], v[156:159], v[212:215], v[80:83]
	v_mfma_f32_16x16x32_bf16 v[72:75], v[164:167], v[212:215], v[72:75]
	s_setprio 0
	s_setprio 1
	v_mfma_f32_16x16x32_bf16 v[116:119], v[168:171], v[184:187], v[116:119]
	v_mfma_f32_16x16x32_bf16 v[108:111], v[176:179], v[184:187], v[108:111]
	v_mfma_f32_16x16x32_bf16 v[100:103], v[168:171], v[192:195], v[100:103]
	v_mfma_f32_16x16x32_bf16 v[92:95], v[176:179], v[192:195], v[92:95]
	v_mfma_f32_16x16x32_bf16 v[84:87], v[168:171], v[200:203], v[84:87]
	v_mfma_f32_16x16x32_bf16 v[76:79], v[176:179], v[200:203], v[76:79]
	v_mfma_f32_16x16x32_bf16 v[68:71], v[168:171], v[208:211], v[68:71]
	v_mfma_f32_16x16x32_bf16 v[64:67], v[176:179], v[208:211], v[64:67]
	v_mfma_f32_16x16x32_bf16 v[116:119], v[172:175], v[188:191], v[116:119]
	v_mfma_f32_16x16x32_bf16 v[108:111], v[180:183], v[188:191], v[108:111]
	v_mfma_f32_16x16x32_bf16 v[100:103], v[172:175], v[196:199], v[100:103]
	v_mfma_f32_16x16x32_bf16 v[92:95], v[180:183], v[196:199], v[92:95]
	v_mfma_f32_16x16x32_bf16 v[84:87], v[172:175], v[204:207], v[84:87]
	v_mfma_f32_16x16x32_bf16 v[76:79], v[180:183], v[204:207], v[76:79]
	v_mfma_f32_16x16x32_bf16 v[68:71], v[172:175], v[212:215], v[68:71]
	v_mfma_f32_16x16x32_bf16 v[64:67], v[180:183], v[212:215], v[64:67]
	s_setprio 0
	s_barrier
; #define PG8_STAGE(bufoff, gbase, voff) do { const char* sb_ = (gbase); _Pragma("unroll") for (int _i = 0; _i < 2; ++_i) PG8_GLDS(sb_, (voff)[_i], bufoff, _i); } while (0)
; #define PG8_LDA(dst, b, h) do { if constexpr (F8) { _Pragma("unroll") for (int m = 0; m < 4; ++m) dst##8[m] = PG8_RD8(lds + PG8_SA(b, h) + aoff + m * 2048); } else { \
;         _Pragma("unroll") for (int m = 0; m < 4; ++m) _Pragma("unroll") for (int k = 0; k < 2; ++k) dst[m][k] = *(const PG8_LAS bf16x8*)(lds + PG8_SA(b, h) + aoff + m * 2048 + k * 1024); } } while (0)
; #define PG8_LDB(dst, b, h) do { if constexpr (F8) { _Pragma("unroll") for (int n = 0; n < 2; ++n) dst##8[n] = PG8_RD8(lds + PG8_SB(b, h) + boff + n * 2048); } else { \
;         _Pragma("unroll") for (int n = 0; n < 2; ++n) _Pragma("unroll") for (int k = 0; k < 2; ++k) dst[n][k] = *(const PG8_LAS bf16x8*)(lds + PG8_SB(b, h) + boff + n * 2048 + k * 1024); } } while (0)
; #define PG8_WAIT_V(n) asm volatile("s_waitcnt vmcnt(" #n ")" ::: "memory")
;     ...
;         for (int t = 0; t < nt; t += 2) {
;             const bool last = (t == nt - 2);
;             const size_t k1 = (size_t)(t + 1) * kstep;
;             const size_t k2 = last ? 0 : (size_t)(t + 2) * kstep, k3 = k2 + kstep;
;             const char* b2 = last ? nB : cB + (size_t)(t + 2) * kstep; const char* b3 = b2 + kstep;
;             PG8_LDB(B0, 0, 0); PG8_LDB(B1, 0, 1); PG8_SCHED; PG8_LDA(At, 0, 0); PG8_STAGE_A(PG8_SA(1, 1), 1, k1, false);
;             PG8_WAIT_V(8); PG8_WAIT_L(0); PG8_BAR; PG8_MMA(0, 0, At, B0); PG8_MMA(0, 1, At, B1); PG8_BAR; PG8_SCHED;
;             PG8_LDA(At, 0, 1); PG8_STAGE(PG8_SB(0, 0), b2, voffB); PG8_STAGE(PG8_SB(0, 1), b2 + hstep, voffB); PG8_STAGE_A(PG8_SA(0, 0), 0, k2, last);
;             PG8_WAIT_V(8); PG8_WAIT_L(0); PG8_BAR; PG8_MMA(1, 0, At, B0); PG8_MMA(1, 1, At, B1); PG8_BAR; PG8_SCHED;
;             PG8_LDB(B0, 1, 0); PG8_LDB(B1, 1, 1); PG8_SCHED; PG8_LDA(At, 1, 0); PG8_STAGE_A(PG8_SA(0, 1), 1, k2, last);
;             PG8_WAIT_V(8); PG8_WAIT_L(0); PG8_BAR; PG8_MMA(0, 0, At, B0); PG8_MMA(0, 1, At, B1); PG8_BAR; PG8_SCHED;
;             PG8_LDA(At, 1, 1); PG8_STAGE(PG8_SB(1, 0), b3, voffB); PG8_STAGE(PG8_SB(1, 1), b3 + hstep, voffB); PG8_STAGE_A(PG8_SA(1, 0), 0, k3, last);
;             PG8_WAIT_V(8); PG8_WAIT_L(0); PG8_BAR; PG8_MMA(1, 0, At, B0); PG8_MMA(1, 1, At, B1); PG8_BAR; PG8_SCHED;
;         }
	s_add_i32 s34, s40, s57
	v_lshl_add_u64 v[216:217], v[216:217], 0, s[8:9]
	s_mov_b32 m0, s34
	ds_read_b128 v[184:187], v151 offset:49152
	ds_read_b128 v[188:191], v151 offset:50176
	ds_read_b128 v[192:195], v151 offset:51200
	ds_read_b128 v[196:199], v151 offset:52224
	ds_read_b128 v[200:203], v151 offset:53248
	ds_read_b128 v[204:207], v151 offset:54272
	ds_read_b128 v[208:211], v151 offset:55296
	ds_read_b128 v[212:215], v151 offset:56320
	global_load_lds_dwordx4 v[216:217], off
	s_add_i32 m0, s34, 0x2000
	s_add_u32 s34, s38, 0x80080
	v_lshl_add_u64 v[216:217], v[218:219], 0, s[8:9]
	s_addc_u32 s35, s39, 0
	s_add_i32 s38, s41, s57
	global_load_lds_dwordx4 v[216:217], off
	v_lshl_add_u64 v[216:217], s[34:35], 0, v[130:131]
	s_mov_b32 m0, s38
	s_nop 0
	global_load_lds_dwordx4 v[216:217], off
	v_lshl_add_u64 v[216:217], s[34:35], 0, v[134:135]
	s_add_i32 m0, s38, 0x2000
	s_nop 0
	global_load_lds_dwordx4 v[216:217], off
	v_lshl_add_u64 v[216:217], v[220:221], 0, s[8:9]
	s_mov_b32 m0, s64
	s_nop 0
	global_load_lds_dwordx4 v[216:217], off
	v_lshl_add_u64 v[216:217], v[222:223], 0, s[8:9]
	s_mov_b32 m0, s65
	s_nop 0
	global_load_lds_dwordx4 v[216:217], off
	s_waitcnt vmcnt(8)
	s_waitcnt lgkmcnt(0)
	s_barrier
	s_setprio 1
	v_mfma_f32_16x16x32_bf16 v[60:63], v[152:155], v[184:187], v[60:63]
	v_mfma_f32_16x16x32_bf16 v[56:59], v[160:163], v[184:187], v[56:59]
	v_mfma_f32_16x16x32_bf16 v[52:55], v[152:155], v[192:195], v[52:55]
	v_mfma_f32_16x16x32_bf16 v[44:47], v[160:163], v[192:195], v[44:47]
	v_mfma_f32_16x16x32_bf16 v[36:39], v[152:155], v[200:203], v[36:39]
	v_mfma_f32_16x16x32_bf16 v[28:31], v[160:163], v[200:203], v[28:31]
	v_mfma_f32_16x16x32_bf16 v[20:23], v[152:155], v[208:211], v[20:23]
	v_mfma_f32_16x16x32_bf16 v[12:15], v[160:163], v[208:211], v[12:15]
	v_mfma_f32_16x16x32_bf16 v[60:63], v[156:159], v[188:191], v[60:63]
	v_mfma_f32_16x16x32_bf16 v[56:59], v[164:167], v[188:191], v[56:59]
	v_mfma_f32_16x16x32_bf16 v[52:55], v[156:159], v[196:199], v[52:55]
	v_mfma_f32_16x16x32_bf16 v[44:47], v[164:167], v[196:199], v[44:47]
	v_mfma_f32_16x16x32_bf16 v[36:39], v[156:159], v[204:207], v[36:39]
	v_mfma_f32_16x16x32_bf16 v[28:31], v[164:167], v[204:207], v[28:31]
	v_mfma_f32_16x16x32_bf16 v[20:23], v[156:159], v[212:215], v[20:23]
	v_mfma_f32_16x16x32_bf16 v[12:15], v[164:167], v[212:215], v[12:15]
	s_setprio 0
	s_setprio 1
	v_mfma_f32_16x16x32_bf16 v[48:51], v[168:171], v[184:187], v[48:51]
	v_mfma_f32_16x16x32_bf16 v[40:43], v[176:179], v[184:187], v[40:43]
	v_mfma_f32_16x16x32_bf16 v[32:35], v[168:171], v[192:195], v[32:35]
	v_mfma_f32_16x16x32_bf16 v[24:27], v[176:179], v[192:195], v[24:27]
	v_mfma_f32_16x16x32_bf16 v[16:19], v[168:171], v[200:203], v[16:19]
	v_mfma_f32_16x16x32_bf16 v[8:11], v[176:179], v[200:203], v[8:11]
	v_mfma_f32_16x16x32_bf16 v[4:7], v[168:171], v[208:211], v[4:7]
	v_mfma_f32_16x16x32_bf16 v[0:3], v[176:179], v[208:211], v[0:3]
	v_mfma_f32_16x16x32_bf16 v[48:51], v[172:175], v[188:191], v[48:51]
	v_mfma_f32_16x16x32_bf16 v[40:43], v[180:183], v[188:191], v[40:43]
	v_mfma_f32_16x16x32_bf16 v[32:35], v[172:175], v[196:199], v[32:35]
	v_mfma_f32_16x16x32_bf16 v[24:27], v[180:183], v[196:199], v[24:27]
	v_mfma_f32_16x16x32_bf16 v[16:19], v[172:175], v[204:207], v[16:19]
	v_mfma_f32_16x16x32_bf16 v[8:11], v[180:183], v[204:207], v[8:11]
	v_mfma_f32_16x16x32_bf16 v[4:7], v[172:175], v[212:215], v[4:7]
	v_mfma_f32_16x16x32_bf16 v[0:3], v[180:183], v[212:215], v[0:3]
	s_setprio 0
	s_barrier
	s_add_i32 s79, s79, 2
	s_cmp_gt_u32 s79, 29
	s_mov_b64 s[34:35], s[36:37]
	s_cbranch_scc0 .LBB4_1055
	s_and_b64 vcc, exec, s[10:11]
	s_cbranch_vccz .LBB4_1058
	s_barrier

; #define PG8_STAGE(bufoff, gbase, voff) do { const char* sb_ = (gbase); _Pragma("unroll") for (int _i = 0; _i < 2; ++_i) PG8_GLDS(sb_, (voff)[_i], bufoff, _i); } while (0)
; #define PG8_LDA(dst, b, h) do { if constexpr (F8) { _Pragma("unroll") for (int m = 0; m < 4; ++m) dst##8[m] = PG8_RD8(lds + PG8_SA(b, h) + aoff + m * 2048); } else { \
;         _Pragma("unroll") for (int m = 0; m < 4; ++m) _Pragma("unroll") for (int k = 0; k < 2; ++k) dst[m][k] = *(const PG8_LAS bf16x8*)(lds + PG8_SA(b, h) + aoff + m * 2048 + k * 1024); } } while (0)
; #define PG8_LDB(dst, b, h) do { if constexpr (F8) { _Pragma("unroll") for (int n = 0; n < 2; ++n) dst##8[n] = PG8_RD8(lds + PG8_SB(b, h) + boff + n * 2048); } else { \
;         _Pragma("unroll") for (int n = 0; n < 2; ++n) _Pragma("unroll") for (int k = 0; k < 2; ++k) dst[n][k] = *(const PG8_LAS bf16x8*)(lds + PG8_SB(b, h) + boff + n * 2048 + k * 1024); } } while (0)
; #define PG8_WAIT_V(n) asm volatile("s_waitcnt vmcnt(" #n ")" ::: "memory")
;     ...
;         for (int t = 0; t < nt; t += 2) {
;             const bool last = (t == nt - 2);
;             const size_t k1 = (size_t)(t + 1) * kstep;
;             const size_t k2 = last ? 0 : (size_t)(t + 2) * kstep, k3 = k2 + kstep;
;             const char* b2 = last ? nB : cB + (size_t)(t + 2) * kstep; const char* b3 = b2 + kstep;
;             PG8_LDB(B0, 0, 0); PG8_LDB(B1, 0, 1); PG8_SCHED; PG8_LDA(At, 0, 0); PG8_STAGE_A(PG8_SA(1, 1), 1, k1, false);
;             PG8_WAIT_V(8); PG8_WAIT_L(0); PG8_BAR; PG8_MMA(0, 0, At, B0); PG8_MMA(0, 1, At, B1); PG8_BAR; PG8_SCHED;
;             PG8_LDA(At, 0, 1); PG8_STAGE(PG8_SB(0, 0), b2, voffB); PG8_STAGE(PG8_SB(0, 1), b2 + hstep, voffB); PG8_STAGE_A(PG8_SA(0, 0), 0, k2, last);
;             PG8_WAIT_V(8); PG8_WAIT_L(0); PG8_BAR; PG8_MMA(1, 0, At, B0); PG8_MMA(1, 1, At, B1); PG8_BAR; PG8_SCHED;
;             PG8_LDB(B0, 1, 0); PG8_LDB(B1, 1, 1); PG8_SCHED; PG8_LDA(At, 1, 0); PG8_STAGE_A(PG8_SA(0, 1), 1, k2, last);
;             PG8_WAIT_V(8); PG8_WAIT_L(0); PG8_BAR; PG8_MMA(0, 0, At, B0); PG8_MMA(0, 1, At, B1); PG8_BAR; PG8_SCHED;
;             PG8_LDA(At, 1, 1); PG8_STAGE(PG8_SB(1, 0), b3, voffB); PG8_STAGE(PG8_SB(1, 1), b3 + hstep, voffB); PG8_STAGE_A(PG8_SA(1, 0), 0, k3, last);
;             PG8_WAIT_V(8); PG8_WAIT_L(0); PG8_BAR; PG8_MMA(1, 0, At, B0); PG8_MMA(1, 1, At, B1); PG8_BAR; PG8_SCHED;
;         }
.LBB4_1452:
	ds_read_b128 v[146:149], v138
	ds_read_b128 v[150:153], v138 offset:16
	ds_read_b128 v[154:157], v138 offset:2048
	ds_read_b128 v[158:161], v138 offset:2064
	ds_read_b128 v[162:165], v139
	ds_read_b128 v[166:169], v139 offset:16
	ds_read_b128 v[170:173], v139 offset:2048
	ds_read_b128 v[174:177], v139 offset:2064
	s_add_u32 s28, s20, s24
	s_addc_u32 s29, s21, s25
	s_cmp_eq_u32 s15, 12
	s_cselect_b64 s[30:31], -1, 0
	s_and_b64 s[26:27], s[30:31], exec
	s_cselect_b32 s82, 0, s24
	s_cselect_b32 s27, s17, s29
	s_cselect_b32 s26, s16, s28
	ds_read_b128 v[178:181], v140
	ds_read_b128 v[182:185], v140 offset:16
	ds_read_b128 v[186:189], v140 offset:2048
	ds_read_b128 v[190:193], v140 offset:2064
	ds_read_b128 v[194:197], v140 offset:4096
	ds_read_b128 v[198:201], v140 offset:4112
	ds_read_b128 v[202:205], v140 offset:6144
	ds_read_b128 v[206:209], v140 offset:6160
	ds_read2st64_b32 v[128:129], v132 offset0:16 offset1:24
	s_add_u32 s28, s6, s24
	s_addc_u32 s29, s7, s25
	s_add_u32 s28, s28, 0xffffff80
	s_addc_u32 s29, s29, -1
	s_waitcnt lgkmcnt(0)
	s_mov_b32 m0, s66
	s_nop 0
	global_load_lds_dwordx4 v128, s[28:29]
	s_nop 0
	s_mov_b32 m0, s67
	s_nop 0
	global_load_lds_dwordx4 v129, s[28:29]
	s_waitcnt vmcnt(8)
	s_waitcnt lgkmcnt(0)
	s_barrier
	s_setprio 1
	v_mfma_scale_f32_16x16x128_f8f6f4 v[124:127], v[146:153], v[178:185], v[124:127], v142, v141 op_sel_hi:[0,0,0]
	v_mfma_scale_f32_16x16x128_f8f6f4 v[120:123], v[154:161], v[178:185], v[120:123], v142, v141 op_sel_hi:[0,0,0]
	v_mfma_scale_f32_16x16x128_f8f6f4 v[108:111], v[146:153], v[186:193], v[108:111], v142, v141 op_sel_hi:[0,0,0]
	v_mfma_scale_f32_16x16x128_f8f6f4 v[104:107], v[154:161], v[186:193], v[104:107], v142, v141 op_sel_hi:[0,0,0]
	v_mfma_scale_f32_16x16x128_f8f6f4 v[210:213], v[146:153], v[194:201], v[92:95], v142, v141 op_sel_hi:[0,0,0]
	v_mfma_scale_f32_16x16x128_f8f6f4 v[214:217], v[154:161], v[194:201], v[88:91], v142, v141 op_sel_hi:[0,0,0]
	v_mfma_scale_f32_16x16x128_f8f6f4 v[218:221], v[146:153], v[202:209], v[76:79], v142, v141 op_sel_hi:[0,0,0]
	v_mfma_scale_f32_16x16x128_f8f6f4 v[222:225], v[154:161], v[202:209], v[72:75], v142, v141 op_sel_hi:[0,0,0]
	s_setprio 0
	s_setprio 1
	v_mfma_scale_f32_16x16x128_f8f6f4 v[116:119], v[162:169], v[178:185], v[116:119], v142, v141 op_sel_hi:[0,0,0]
	v_mfma_scale_f32_16x16x128_f8f6f4 v[112:115], v[170:177], v[178:185], v[112:115], v142, v141 op_sel_hi:[0,0,0]
	v_mfma_scale_f32_16x16x128_f8f6f4 v[100:103], v[162:169], v[186:193], v[100:103], v142, v141 op_sel_hi:[0,0,0]
	v_mfma_scale_f32_16x16x128_f8f6f4 v[96:99], v[170:177], v[186:193], v[96:99], v142, v141 op_sel_hi:[0,0,0]
	v_mfma_scale_f32_16x16x128_f8f6f4 v[178:181], v[162:169], v[194:201], v[84:87], v142, v141 op_sel_hi:[0,0,0]
	v_mfma_scale_f32_16x16x128_f8f6f4 v[182:185], v[170:177], v[194:201], v[80:83], v142, v141 op_sel_hi:[0,0,0]
	v_mfma_scale_f32_16x16x128_f8f6f4 v[186:189], v[162:169], v[202:209], v[68:71], v142, v141 op_sel_hi:[0,0,0]
	v_mfma_scale_f32_16x16x128_f8f6f4 v[190:193], v[170:177], v[202:209], v[64:67], v142, v141 op_sel_hi:[0,0,0]
	s_setprio 0
	s_barrier
	s_nop 4
	ds_read_b128 v[64:67], v140 offset:16384
	ds_read_b128 v[68:71], v140 offset:16400
	ds_read_b128 v[72:75], v140 offset:18432
	ds_read_b128 v[76:79], v140 offset:18448
	ds_read_b128 v[80:83], v140 offset:20480
	ds_read_b128 v[84:87], v140 offset:20496
	ds_read_b128 v[88:91], v140 offset:22528
	ds_read_b128 v[92:95], v140 offset:22544
	s_mov_b32 m0, s19
	s_nop 0
	global_load_lds_dwordx4 v135, s[26:27]
	s_add_u32 s28, s26, 0x40000
	s_mov_b32 m0, s42
	s_nop 0
	global_load_lds_dwordx4 v136, s[26:27]
	s_addc_u32 s29, s27, 0
	s_mov_b32 m0, s43
	s_nop 0
	global_load_lds_dwordx4 v135, s[28:29]
	s_nop 0
	s_mov_b32 m0, s54
	s_nop 0
	global_load_lds_dwordx4 v136, s[28:29]
	s_add_u32 s28, s6, s82
	s_addc_u32 s29, s7, 0
	s_and_b64 s[30:31], s[22:23], s[30:31]
	s_and_b64 s[30:31], s[30:31], exec
	s_cselect_b32 s30, s78, s80
	s_lshl_b32 s30, s30, 13
	s_and_b32 s30, s30, 0x2000
	v_add_u32_e32 v133, s30, v137
	ds_read2st64_b32 v[128:129], v133 offset1:8
	s_waitcnt lgkmcnt(0)
	s_mov_b32 m0, s39
	s_nop 0
	global_load_lds_dwordx4 v128, s[28:29]
	s_nop 0
	s_mov_b32 m0, s55
	s_nop 0
	global_load_lds_dwordx4 v129, s[28:29]
	s_waitcnt vmcnt(8)
	s_waitcnt lgkmcnt(0)
	s_barrier
	s_setprio 1
	v_mfma_scale_f32_16x16x128_f8f6f4 v[60:63], v[146:153], v[64:71], v[60:63], v142, v141 op_sel_hi:[0,0,0]
	v_mfma_scale_f32_16x16x128_f8f6f4 v[56:59], v[154:161], v[64:71], v[56:59], v142, v141 op_sel_hi:[0,0,0]
	v_mfma_scale_f32_16x16x128_f8f6f4 v[194:197], v[146:153], v[72:79], v[44:47], v142, v141 op_sel_hi:[0,0,0]
	v_mfma_scale_f32_16x16x128_f8f6f4 v[198:201], v[154:161], v[72:79], v[40:43], v142, v141 op_sel_hi:[0,0,0]
	v_mfma_scale_f32_16x16x128_f8f6f4 v[202:205], v[146:153], v[80:87], v[28:31], v142, v141 op_sel_hi:[0,0,0]
	v_mfma_scale_f32_16x16x128_f8f6f4 v[206:209], v[154:161], v[80:87], v[24:27], v142, v141 op_sel_hi:[0,0,0]
	v_mfma_scale_f32_16x16x128_f8f6f4 v[226:229], v[146:153], v[88:95], v[12:15], v142, v141 op_sel_hi:[0,0,0]
	v_mfma_scale_f32_16x16x128_f8f6f4 v[230:233], v[154:161], v[88:95], v[8:11], v142, v141 op_sel_hi:[0,0,0]
	s_setprio 0
	s_setprio 1
	v_mfma_scale_f32_16x16x128_f8f6f4 v[52:55], v[162:169], v[64:71], v[52:55], v142, v141 op_sel_hi:[0,0,0]
	v_mfma_scale_f32_16x16x128_f8f6f4 v[48:51], v[170:177], v[64:71], v[48:51], v142, v141 op_sel_hi:[0,0,0]
	v_mfma_scale_f32_16x16x128_f8f6f4 v[234:237], v[162:169], v[72:79], v[36:39], v142, v141 op_sel_hi:[0,0,0]
	v_mfma_scale_f32_16x16x128_f8f6f4 v[238:241], v[170:177], v[72:79], v[32:35], v142, v141 op_sel_hi:[0,0,0]
	v_mfma_scale_f32_16x16x128_f8f6f4 v[242:245], v[162:169], v[80:87], v[20:23], v142, v141 op_sel_hi:[0,0,0]
	v_mfma_scale_f32_16x16x128_f8f6f4 v[246:249], v[170:177], v[80:87], v[16:19], v142, v141 op_sel_hi:[0,0,0]
	v_mfma_scale_f32_16x16x128_f8f6f4 v[250:253], v[162:169], v[88:95], v[4:7], v142, v141 op_sel_hi:[0,0,0]
	v_mfma_scale_f32_16x16x128_f8f6f4 v[128:131], v[170:177], v[88:95], v[0:3], v142, v141 op_sel_hi:[0,0,0]
	s_setprio 0
	s_barrier
; #define PG8_STAGE(bufoff, gbase, voff) do { const char* sb_ = (gbase); _Pragma("unroll") for (int _i = 0; _i < 2; ++_i) PG8_GLDS(sb_, (voff)[_i], bufoff, _i); } while (0)
; #define PG8_LDA(dst, b, h) do { if constexpr (F8) { _Pragma("unroll") for (int m = 0; m < 4; ++m) dst##8[m] = PG8_RD8(lds + PG8_SA(b, h) + aoff + m * 2048); } else { \
;         _Pragma("unroll") for (int m = 0; m < 4; ++m) _Pragma("unroll") for (int k = 0; k < 2; ++k) dst[m][k] = *(const PG8_LAS bf16x8*)(lds + PG8_SA(b, h) + aoff + m * 2048 + k * 1024); } } while (0)
; #define PG8_LDB(dst, b, h) do { if constexpr (F8) { _Pragma("unroll") for (int n = 0; n < 2; ++n) dst##8[n] = PG8_RD8(lds + PG8_SB(b, h) + boff + n * 2048); } else { \
;         _Pragma("unroll") for (int n = 0; n < 2; ++n) _Pragma("unroll") for (int k = 0; k < 2; ++k) dst[n][k] = *(const PG8_LAS bf16x8*)(lds + PG8_SB(b, h) + boff + n * 2048 + k * 1024); } } while (0)
; #define PG8_WAIT_V(n) asm volatile("s_waitcnt vmcnt(" #n ")" ::: "memory")
;     ...
;         for (int t = 0; t < nt; t += 2) {
;             const bool last = (t == nt - 2);
;             const size_t k1 = (size_t)(t + 1) * kstep;
;             const size_t k2 = last ? 0 : (size_t)(t + 2) * kstep, k3 = k2 + kstep;
;             const char* b2 = last ? nB : cB + (size_t)(t + 2) * kstep; const char* b3 = b2 + kstep;
;             PG8_LDB(B0, 0, 0); PG8_LDB(B1, 0, 1); PG8_SCHED; PG8_LDA(At, 0, 0); PG8_STAGE_A(PG8_SA(1, 1), 1, k1, false);
;             PG8_WAIT_V(8); PG8_WAIT_L(0); PG8_BAR; PG8_MMA(0, 0, At, B0); PG8_MMA(0, 1, At, B1); PG8_BAR; PG8_SCHED;
;             PG8_LDA(At, 0, 1); PG8_STAGE(PG8_SB(0, 0), b2, voffB); PG8_STAGE(PG8_SB(0, 1), b2 + hstep, voffB); PG8_STAGE_A(PG8_SA(0, 0), 0, k2, last);
;             PG8_WAIT_V(8); PG8_WAIT_L(0); PG8_BAR; PG8_MMA(1, 0, At, B0); PG8_MMA(1, 1, At, B1); PG8_BAR; PG8_SCHED;
;             PG8_LDB(B0, 1, 0); PG8_LDB(B1, 1, 1); PG8_SCHED; PG8_LDA(At, 1, 0); PG8_STAGE_A(PG8_SA(0, 1), 1, k2, last);
;             PG8_WAIT_V(8); PG8_WAIT_L(0); PG8_BAR; PG8_MMA(0, 0, At, B0); PG8_MMA(0, 1, At, B1); PG8_BAR; PG8_SCHED;
;             PG8_LDA(At, 1, 1); PG8_STAGE(PG8_SB(1, 0), b3, voffB); PG8_STAGE(PG8_SB(1, 1), b3 + hstep, voffB); PG8_STAGE_A(PG8_SA(1, 0), 0, k3, last);
;             PG8_WAIT_V(8); PG8_WAIT_L(0); PG8_BAR; PG8_MMA(1, 0, At, B0); PG8_MMA(1, 1, At, B1); PG8_BAR; PG8_SCHED;
;         }
	s_nop 4
	ds_read_b128 v[0:3], v143
	ds_read_b128 v[4:7], v143 offset:16
	ds_read_b128 v[16:19], v143 offset:2048
	ds_read_b128 v[20:23], v143 offset:2064
	ds_read_b128 v[146:149], v144
	ds_read_b128 v[150:153], v144 offset:16
	ds_read_b128 v[154:157], v144 offset:2048
	ds_read_b128 v[158:161], v144 offset:2064
	ds_read_b128 v[8:11], v140 offset:32768
	ds_read_b128 v[12:15], v140 offset:32784
	ds_read_b128 v[24:27], v140 offset:34816
	ds_read_b128 v[28:31], v140 offset:34832
	ds_read2st64_b32 v[64:65], v133 offset0:16 offset1:24
	ds_read_b128 v[32:35], v140 offset:36864
	ds_read_b128 v[36:39], v140 offset:36880
	ds_read_b128 v[40:43], v140 offset:38912
	ds_read_b128 v[44:47], v140 offset:38928
	s_waitcnt lgkmcnt(4)
	s_mov_b32 m0, s56
	s_nop 0
	global_load_lds_dwordx4 v64, s[28:29]
	s_nop 0
	s_mov_b32 m0, s57
	s_nop 0
	global_load_lds_dwordx4 v65, s[28:29]
	s_waitcnt vmcnt(8)
	s_waitcnt lgkmcnt(0)
	s_barrier
	s_setprio 1
	v_mfma_scale_f32_16x16x128_f8f6f4 v[124:127], v[0:7], v[8:15], v[124:127], v142, v141 op_sel_hi:[0,0,0]
	v_mfma_scale_f32_16x16x128_f8f6f4 v[120:123], v[16:23], v[8:15], v[120:123], v142, v141 op_sel_hi:[0,0,0]
	v_mfma_scale_f32_16x16x128_f8f6f4 v[108:111], v[0:7], v[24:31], v[108:111], v142, v141 op_sel_hi:[0,0,0]
	v_mfma_scale_f32_16x16x128_f8f6f4 v[104:107], v[16:23], v[24:31], v[104:107], v142, v141 op_sel_hi:[0,0,0]
	v_mfma_scale_f32_16x16x128_f8f6f4 v[92:95], v[0:7], v[32:39], v[210:213], v142, v141 op_sel_hi:[0,0,0]
	v_mfma_scale_f32_16x16x128_f8f6f4 v[88:91], v[16:23], v[32:39], v[214:217], v142, v141 op_sel_hi:[0,0,0]
	v_mfma_scale_f32_16x16x128_f8f6f4 v[76:79], v[0:7], v[40:47], v[218:221], v142, v141 op_sel_hi:[0,0,0]
	v_mfma_scale_f32_16x16x128_f8f6f4 v[72:75], v[16:23], v[40:47], v[222:225], v142, v141 op_sel_hi:[0,0,0]
	s_setprio 0
	s_setprio 1
	v_mfma_scale_f32_16x16x128_f8f6f4 v[116:119], v[146:153], v[8:15], v[116:119], v142, v141 op_sel_hi:[0,0,0]
	v_mfma_scale_f32_16x16x128_f8f6f4 v[112:115], v[154:161], v[8:15], v[112:115], v142, v141 op_sel_hi:[0,0,0]
	v_mfma_scale_f32_16x16x128_f8f6f4 v[100:103], v[146:153], v[24:31], v[100:103], v142, v141 op_sel_hi:[0,0,0]
	v_mfma_scale_f32_16x16x128_f8f6f4 v[96:99], v[154:161], v[24:31], v[96:99], v142, v141 op_sel_hi:[0,0,0]
	v_mfma_scale_f32_16x16x128_f8f6f4 v[84:87], v[146:153], v[32:39], v[178:181], v142, v141 op_sel_hi:[0,0,0]
	v_mfma_scale_f32_16x16x128_f8f6f4 v[80:83], v[154:161], v[32:39], v[182:185], v142, v141 op_sel_hi:[0,0,0]
	v_mfma_scale_f32_16x16x128_f8f6f4 v[68:71], v[146:153], v[40:47], v[186:189], v142, v141 op_sel_hi:[0,0,0]
	v_mfma_scale_f32_16x16x128_f8f6f4 v[64:67], v[154:161], v[40:47], v[190:193], v142, v141 op_sel_hi:[0,0,0]
	s_setprio 0
	s_barrier
	ds_read_b128 v[32:35], v140 offset:49152
	ds_read_b128 v[36:39], v140 offset:49168
	ds_read_b128 v[162:165], v140 offset:51200
	ds_read_b128 v[166:169], v140 offset:51216
	ds_read_b128 v[170:173], v140 offset:53248
	ds_read_b128 v[174:177], v140 offset:53264
	ds_read_b128 v[178:181], v140 offset:55296
	ds_read_b128 v[182:185], v140 offset:55312
	s_add_u32 s30, s26, 0x80
	s_addc_u32 s31, s27, 0
	s_mov_b32 m0, s60
	s_nop 0
	global_load_lds_dwordx4 v135, s[30:31]
	s_add_u32 s26, s26, 0x40080
	s_mov_b32 m0, s61
	s_nop 0
	global_load_lds_dwordx4 v136, s[30:31]
	s_addc_u32 s27, s27, 0
	s_mov_b32 m0, s64
	s_nop 0
	global_load_lds_dwordx4 v135, s[26:27]
	s_nop 0
	s_mov_b32 m0, s65
	s_nop 0
	global_load_lds_dwordx4 v136, s[26:27]
	s_add_u32 s26, s28, 0x80
	ds_read2st64_b32 v[8:9], v133 offset1:8
	s_addc_u32 s27, s29, 0
	s_waitcnt lgkmcnt(0)
	s_mov_b32 m0, s62
	s_nop 0
	global_load_lds_dwordx4 v8, s[26:27]
	s_nop 0
	s_mov_b32 m0, s63
	s_nop 0
	global_load_lds_dwordx4 v9, s[26:27]
	s_waitcnt vmcnt(8)
	s_waitcnt lgkmcnt(0)
	s_barrier
	s_setprio 1
	v_mfma_scale_f32_16x16x128_f8f6f4 v[60:63], v[0:7], v[32:39], v[60:63], v142, v141 op_sel_hi:[0,0,0]
	v_mfma_scale_f32_16x16x128_f8f6f4 v[56:59], v[16:23], v[32:39], v[56:59], v142, v141 op_sel_hi:[0,0,0]
	v_mfma_scale_f32_16x16x128_f8f6f4 v[44:47], v[0:7], v[162:169], v[194:197], v142, v141 op_sel_hi:[0,0,0]
	v_mfma_scale_f32_16x16x128_f8f6f4 v[40:43], v[16:23], v[162:169], v[198:201], v142, v141 op_sel_hi:[0,0,0]
	v_mfma_scale_f32_16x16x128_f8f6f4 v[28:31], v[0:7], v[170:177], v[202:205], v142, v141 op_sel_hi:[0,0,0]
	v_mfma_scale_f32_16x16x128_f8f6f4 v[24:27], v[16:23], v[170:177], v[206:209], v142, v141 op_sel_hi:[0,0,0]
	v_mfma_scale_f32_16x16x128_f8f6f4 v[12:15], v[0:7], v[178:185], v[226:229], v142, v141 op_sel_hi:[0,0,0]
	v_mfma_scale_f32_16x16x128_f8f6f4 v[8:11], v[16:23], v[178:185], v[230:233], v142, v141 op_sel_hi:[0,0,0]
	s_setprio 0
	s_setprio 1
	v_mfma_scale_f32_16x16x128_f8f6f4 v[52:55], v[146:153], v[32:39], v[52:55], v142, v141 op_sel_hi:[0,0,0]
	v_mfma_scale_f32_16x16x128_f8f6f4 v[48:51], v[154:161], v[32:39], v[48:51], v142, v141 op_sel_hi:[0,0,0]
	v_mfma_scale_f32_16x16x128_f8f6f4 v[36:39], v[146:153], v[162:169], v[234:237], v142, v141 op_sel_hi:[0,0,0]
	v_mfma_scale_f32_16x16x128_f8f6f4 v[32:35], v[154:161], v[162:169], v[238:241], v142, v141 op_sel_hi:[0,0,0]
	v_mfma_scale_f32_16x16x128_f8f6f4 v[20:23], v[146:153], v[170:177], v[242:245], v142, v141 op_sel_hi:[0,0,0]
	v_mfma_scale_f32_16x16x128_f8f6f4 v[16:19], v[154:161], v[170:177], v[246:249], v142, v141 op_sel_hi:[0,0,0]
	v_mfma_scale_f32_16x16x128_f8f6f4 v[4:7], v[146:153], v[178:185], v[250:253], v142, v141 op_sel_hi:[0,0,0]
	v_mfma_scale_f32_16x16x128_f8f6f4 v[0:3], v[154:161], v[178:185], v[128:131], v142, v141 op_sel_hi:[0,0,0]
	s_setprio 0
	s_barrier
	s_add_i32 s15, s15, 2
	s_add_u32 s24, s24, 0x100
	s_addc_u32 s25, s25, 0
	s_cmp_gt_u32 s15, 13
	s_cbranch_scc0 .LBB4_1452
	s_and_b64 vcc, exec, s[12:13]
	s_cbranch_vccz .LBB4_1455
	s_barrier

; #define PG8_STAGE(bufoff, gbase, voff) do { const char* sb_ = (gbase); _Pragma("unroll") for (int _i = 0; _i < 2; ++_i) PG8_GLDS(sb_, (voff)[_i], bufoff, _i); } while (0)
; #define PG8_LDA(dst, b, h) do { if constexpr (F8) { _Pragma("unroll") for (int m = 0; m < 4; ++m) dst##8[m] = PG8_RD8(lds + PG8_SA(b, h) + aoff + m * 2048); } else { \
;         _Pragma("unroll") for (int m = 0; m < 4; ++m) _Pragma("unroll") for (int k = 0; k < 2; ++k) dst[m][k] = *(const PG8_LAS bf16x8*)(lds + PG8_SA(b, h) + aoff + m * 2048 + k * 1024); } } while (0)
; #define PG8_LDB(dst, b, h) do { if constexpr (F8) { _Pragma("unroll") for (int n = 0; n < 2; ++n) dst##8[n] = PG8_RD8(lds + PG8_SB(b, h) + boff + n * 2048); } else { \
;         _Pragma("unroll") for (int n = 0; n < 2; ++n) _Pragma("unroll") for (int k = 0; k < 2; ++k) dst[n][k] = *(const PG8_LAS bf16x8*)(lds + PG8_SB(b, h) + boff + n * 2048 + k * 1024); } } while (0)
; #define PG8_WAIT_V(n) asm volatile("s_waitcnt vmcnt(" #n ")" ::: "memory")
;     ...
;         for (int t = 0; t < nt; t += 2) {
;             const bool last = (t == nt - 2);
;             const size_t k1 = (size_t)(t + 1) * kstep;
;             const size_t k2 = last ? 0 : (size_t)(t + 2) * kstep, k3 = k2 + kstep;
;             const char* b2 = last ? nB : cB + (size_t)(t + 2) * kstep; const char* b3 = b2 + kstep;
;             PG8_LDB(B0, 0, 0); PG8_LDB(B1, 0, 1); PG8_SCHED; PG8_LDA(At, 0, 0); PG8_STAGE_A(PG8_SA(1, 1), 1, k1, false);
;             PG8_WAIT_V(8); PG8_WAIT_L(0); PG8_BAR; PG8_MMA(0, 0, At, B0); PG8_MMA(0, 1, At, B1); PG8_BAR; PG8_SCHED;
;             PG8_LDA(At, 0, 1); PG8_STAGE(PG8_SB(0, 0), b2, voffB); PG8_STAGE(PG8_SB(0, 1), b2 + hstep, voffB); PG8_STAGE_A(PG8_SA(0, 0), 0, k2, last);
;             PG8_WAIT_V(8); PG8_WAIT_L(0); PG8_BAR; PG8_MMA(1, 0, At, B0); PG8_MMA(1, 1, At, B1); PG8_BAR; PG8_SCHED;
;             PG8_LDB(B0, 1, 0); PG8_LDB(B1, 1, 1); PG8_SCHED; PG8_LDA(At, 1, 0); PG8_STAGE_A(PG8_SA(0, 1), 1, k2, last);
;             PG8_WAIT_V(8); PG8_WAIT_L(0); PG8_BAR; PG8_MMA(0, 0, At, B0); PG8_MMA(0, 1, At, B1); PG8_BAR; PG8_SCHED;
;             PG8_LDA(At, 1, 1); PG8_STAGE(PG8_SB(1, 0), b3, voffB); PG8_STAGE(PG8_SB(1, 1), b3 + hstep, voffB); PG8_STAGE_A(PG8_SA(1, 0), 0, k3, last);
;             PG8_WAIT_V(8); PG8_WAIT_L(0); PG8_BAR; PG8_MMA(1, 0, At, B0); PG8_MMA(1, 1, At, B1); PG8_BAR; PG8_SCHED;
;         }
.LBB4_1541:
	ds_read_b128 v[130:133], v146
	ds_read_b128 v[134:137], v146 offset:16
	ds_read_b128 v[154:157], v146 offset:2048
	ds_read_b128 v[158:161], v146 offset:2064
	ds_read_b128 v[162:165], v147
	ds_read_b128 v[166:169], v147 offset:16
	ds_read_b128 v[170:173], v147 offset:2048
	ds_read_b128 v[174:177], v147 offset:2064
	s_add_i32 s25, s40, 0xfffc0080
	s_add_u32 s42, s38, s40
	s_addc_u32 s43, s39, s41
	s_add_u32 s42, s42, 0xfffc0080
	s_addc_u32 s43, s43, -1
	s_add_u32 s54, s36, s40
	s_addc_u32 s55, s37, s41
	s_cmp_eq_u32 s23, 12
	s_cselect_b32 s25, 0, s25
	s_cselect_b32 s43, s31, s43
	s_cselect_b32 s42, s30, s42
	ds_read_b128 v[178:181], v148
	ds_read_b128 v[182:185], v148 offset:16
	ds_read_b128 v[186:189], v148 offset:2048
	ds_read_b128 v[190:193], v148 offset:2064
	ds_read_b128 v[194:197], v148 offset:4096
	ds_read_b128 v[198:201], v148 offset:4112
	ds_read_b128 v[202:205], v148 offset:6144
	ds_read_b128 v[206:209], v148 offset:6160
	s_mov_b32 m0, s80
	s_nop 0
	global_load_lds_dwordx4 v142, s[54:55]
	s_nop 0
	s_mov_b32 m0, s86
	s_nop 0
	global_load_lds_dwordx4 v144, s[54:55]
	s_waitcnt vmcnt(8)
	s_waitcnt lgkmcnt(0)
	s_barrier
	s_setprio 1
	v_mfma_scale_f32_16x16x128_f8f6f4 v[124:127], v[130:137], v[178:185], v[124:127], v150, v149 op_sel_hi:[0,0,0]
	v_mfma_scale_f32_16x16x128_f8f6f4 v[120:123], v[154:161], v[178:185], v[120:123], v150, v149 op_sel_hi:[0,0,0]
	v_mfma_scale_f32_16x16x128_f8f6f4 v[108:111], v[130:137], v[186:193], v[108:111], v150, v149 op_sel_hi:[0,0,0]
	v_mfma_scale_f32_16x16x128_f8f6f4 v[104:107], v[154:161], v[186:193], v[104:107], v150, v149 op_sel_hi:[0,0,0]
	v_mfma_scale_f32_16x16x128_f8f6f4 v[138:141], v[130:137], v[194:201], v[92:95], v150, v149 op_sel_hi:[0,0,0]
	v_mfma_scale_f32_16x16x128_f8f6f4 v[210:213], v[154:161], v[194:201], v[88:91], v150, v149 op_sel_hi:[0,0,0]
	v_mfma_scale_f32_16x16x128_f8f6f4 v[214:217], v[130:137], v[202:209], v[76:79], v150, v149 op_sel_hi:[0,0,0]
	v_mfma_scale_f32_16x16x128_f8f6f4 v[218:221], v[154:161], v[202:209], v[72:75], v150, v149 op_sel_hi:[0,0,0]
	s_setprio 0
	s_setprio 1
	v_mfma_scale_f32_16x16x128_f8f6f4 v[116:119], v[162:169], v[178:185], v[116:119], v150, v149 op_sel_hi:[0,0,0]
	v_mfma_scale_f32_16x16x128_f8f6f4 v[112:115], v[170:177], v[178:185], v[112:115], v150, v149 op_sel_hi:[0,0,0]
	v_mfma_scale_f32_16x16x128_f8f6f4 v[100:103], v[162:169], v[186:193], v[100:103], v150, v149 op_sel_hi:[0,0,0]
	v_mfma_scale_f32_16x16x128_f8f6f4 v[96:99], v[170:177], v[186:193], v[96:99], v150, v149 op_sel_hi:[0,0,0]
	v_mfma_scale_f32_16x16x128_f8f6f4 v[178:181], v[162:169], v[194:201], v[84:87], v150, v149 op_sel_hi:[0,0,0]
	v_mfma_scale_f32_16x16x128_f8f6f4 v[182:185], v[170:177], v[194:201], v[80:83], v150, v149 op_sel_hi:[0,0,0]
	v_mfma_scale_f32_16x16x128_f8f6f4 v[186:189], v[162:169], v[202:209], v[68:71], v150, v149 op_sel_hi:[0,0,0]
	v_mfma_scale_f32_16x16x128_f8f6f4 v[190:193], v[170:177], v[202:209], v[64:67], v150, v149 op_sel_hi:[0,0,0]
	s_setprio 0
	s_barrier
	s_nop 4
	ds_read_b128 v[64:67], v148 offset:16384
	ds_read_b128 v[68:71], v148 offset:16400
	ds_read_b128 v[72:75], v148 offset:18432
	ds_read_b128 v[76:79], v148 offset:18448
	ds_read_b128 v[80:83], v148 offset:20480
	ds_read_b128 v[84:87], v148 offset:20496
	ds_read_b128 v[88:91], v148 offset:22528
	ds_read_b128 v[92:95], v148 offset:22544
	s_mov_b32 m0, s35
	s_nop 0
	global_load_lds_dwordx4 v143, s[42:43]
	s_cselect_b32 s89, s29, s37
	s_mov_b32 m0, s61
	s_nop 0
	global_load_lds_dwordx4 v145, s[42:43]
	s_cselect_b32 s90, s28, s36
	s_add_u32 s54, s42, 0x40000
	s_addc_u32 s55, s43, 0
	s_mov_b32 m0, s62
	s_nop 0
	global_load_lds_dwordx4 v143, s[54:55]
	s_nop 0
	s_mov_b32 m0, s63
	s_nop 0
	global_load_lds_dwordx4 v145, s[54:55]
	s_add_u32 s54, s90, s25
	s_addc_u32 s55, s89, 0
	s_mov_b32 m0, s60
	s_nop 0
	global_load_lds_dwordx4 v142, s[54:55]
	s_nop 0
	s_mov_b32 m0, s64
	s_nop 0
	global_load_lds_dwordx4 v144, s[54:55]
	s_waitcnt vmcnt(8)
	s_waitcnt lgkmcnt(0)
	s_barrier
	s_setprio 1
	v_mfma_scale_f32_16x16x128_f8f6f4 v[60:63], v[130:137], v[64:71], v[60:63], v150, v149 op_sel_hi:[0,0,0]
	v_mfma_scale_f32_16x16x128_f8f6f4 v[56:59], v[154:161], v[64:71], v[56:59], v150, v149 op_sel_hi:[0,0,0]
	v_mfma_scale_f32_16x16x128_f8f6f4 v[194:197], v[130:137], v[72:79], v[44:47], v150, v149 op_sel_hi:[0,0,0]
	v_mfma_scale_f32_16x16x128_f8f6f4 v[198:201], v[154:161], v[72:79], v[40:43], v150, v149 op_sel_hi:[0,0,0]
	v_mfma_scale_f32_16x16x128_f8f6f4 v[202:205], v[130:137], v[80:87], v[28:31], v150, v149 op_sel_hi:[0,0,0]
	v_mfma_scale_f32_16x16x128_f8f6f4 v[206:209], v[154:161], v[80:87], v[24:27], v150, v149 op_sel_hi:[0,0,0]
	v_mfma_scale_f32_16x16x128_f8f6f4 v[222:225], v[130:137], v[88:95], v[12:15], v150, v149 op_sel_hi:[0,0,0]
	v_mfma_scale_f32_16x16x128_f8f6f4 v[226:229], v[154:161], v[88:95], v[8:11], v150, v149 op_sel_hi:[0,0,0]
	s_setprio 0
	s_setprio 1
	v_mfma_scale_f32_16x16x128_f8f6f4 v[52:55], v[162:169], v[64:71], v[52:55], v150, v149 op_sel_hi:[0,0,0]
	v_mfma_scale_f32_16x16x128_f8f6f4 v[48:51], v[170:177], v[64:71], v[48:51], v150, v149 op_sel_hi:[0,0,0]
	v_mfma_scale_f32_16x16x128_f8f6f4 v[230:233], v[162:169], v[72:79], v[36:39], v150, v149 op_sel_hi:[0,0,0]
	v_mfma_scale_f32_16x16x128_f8f6f4 v[234:237], v[170:177], v[72:79], v[32:35], v150, v149 op_sel_hi:[0,0,0]
	v_mfma_scale_f32_16x16x128_f8f6f4 v[238:241], v[162:169], v[80:87], v[20:23], v150, v149 op_sel_hi:[0,0,0]
	v_mfma_scale_f32_16x16x128_f8f6f4 v[242:245], v[170:177], v[80:87], v[16:19], v150, v149 op_sel_hi:[0,0,0]
	v_mfma_scale_f32_16x16x128_f8f6f4 v[246:249], v[162:169], v[88:95], v[4:7], v150, v149 op_sel_hi:[0,0,0]
	v_mfma_scale_f32_16x16x128_f8f6f4 v[250:253], v[170:177], v[88:95], v[0:3], v150, v149 op_sel_hi:[0,0,0]
	s_setprio 0
	s_barrier
; #define PG8_STAGE(bufoff, gbase, voff) do { const char* sb_ = (gbase); _Pragma("unroll") for (int _i = 0; _i < 2; ++_i) PG8_GLDS(sb_, (voff)[_i], bufoff, _i); } while (0)
; #define PG8_LDA(dst, b, h) do { if constexpr (F8) { _Pragma("unroll") for (int m = 0; m < 4; ++m) dst##8[m] = PG8_RD8(lds + PG8_SA(b, h) + aoff + m * 2048); } else { \
;         _Pragma("unroll") for (int m = 0; m < 4; ++m) _Pragma("unroll") for (int k = 0; k < 2; ++k) dst[m][k] = *(const PG8_LAS bf16x8*)(lds + PG8_SA(b, h) + aoff + m * 2048 + k * 1024); } } while (0)
; #define PG8_LDB(dst, b, h) do { if constexpr (F8) { _Pragma("unroll") for (int n = 0; n < 2; ++n) dst##8[n] = PG8_RD8(lds + PG8_SB(b, h) + boff + n * 2048); } else { \
;         _Pragma("unroll") for (int n = 0; n < 2; ++n) _Pragma("unroll") for (int k = 0; k < 2; ++k) dst[n][k] = *(const PG8_LAS bf16x8*)(lds + PG8_SB(b, h) + boff + n * 2048 + k * 1024); } } while (0)
; #define PG8_WAIT_V(n) asm volatile("s_waitcnt vmcnt(" #n ")" ::: "memory")
;     ...
;         for (int t = 0; t < nt; t += 2) {
;             const bool last = (t == nt - 2);
;             const size_t k1 = (size_t)(t + 1) * kstep;
;             const size_t k2 = last ? 0 : (size_t)(t + 2) * kstep, k3 = k2 + kstep;
;             const char* b2 = last ? nB : cB + (size_t)(t + 2) * kstep; const char* b3 = b2 + kstep;
;             PG8_LDB(B0, 0, 0); PG8_LDB(B1, 0, 1); PG8_SCHED; PG8_LDA(At, 0, 0); PG8_STAGE_A(PG8_SA(1, 1), 1, k1, false);
;             PG8_WAIT_V(8); PG8_WAIT_L(0); PG8_BAR; PG8_MMA(0, 0, At, B0); PG8_MMA(0, 1, At, B1); PG8_BAR; PG8_SCHED;
;             PG8_LDA(At, 0, 1); PG8_STAGE(PG8_SB(0, 0), b2, voffB); PG8_STAGE(PG8_SB(0, 1), b2 + hstep, voffB); PG8_STAGE_A(PG8_SA(0, 0), 0, k2, last);
;             PG8_WAIT_V(8); PG8_WAIT_L(0); PG8_BAR; PG8_MMA(1, 0, At, B0); PG8_MMA(1, 1, At, B1); PG8_BAR; PG8_SCHED;
;             PG8_LDB(B0, 1, 0); PG8_LDB(B1, 1, 1); PG8_SCHED; PG8_LDA(At, 1, 0); PG8_STAGE_A(PG8_SA(0, 1), 1, k2, last);
;             PG8_WAIT_V(8); PG8_WAIT_L(0); PG8_BAR; PG8_MMA(0, 0, At, B0); PG8_MMA(0, 1, At, B1); PG8_BAR; PG8_SCHED;
;             PG8_LDA(At, 1, 1); PG8_STAGE(PG8_SB(1, 0), b3, voffB); PG8_STAGE(PG8_SB(1, 1), b3 + hstep, voffB); PG8_STAGE_A(PG8_SA(1, 0), 0, k3, last);
;             PG8_WAIT_V(8); PG8_WAIT_L(0); PG8_BAR; PG8_MMA(1, 0, At, B0); PG8_MMA(1, 1, At, B1); PG8_BAR; PG8_SCHED;
;         }
	s_nop 4
	ds_read_b128 v[0:3], v151
	ds_read_b128 v[4:7], v151 offset:16
	ds_read_b128 v[16:19], v151 offset:2048
	ds_read_b128 v[20:23], v151 offset:2064
	ds_read_b128 v[130:133], v152
	ds_read_b128 v[134:137], v152 offset:16
	ds_read_b128 v[154:157], v152 offset:2048
	ds_read_b128 v[158:161], v152 offset:2064
	ds_read_b128 v[8:11], v148 offset:32768
	ds_read_b128 v[12:15], v148 offset:32784
	ds_read_b128 v[24:27], v148 offset:34816
	ds_read_b128 v[28:31], v148 offset:34832
	ds_read_b128 v[32:35], v148 offset:36864
	ds_read_b128 v[36:39], v148 offset:36880
	ds_read_b128 v[40:43], v148 offset:38912
	ds_read_b128 v[44:47], v148 offset:38928
	s_add_u32 s90, s54, 0x40000
	s_addc_u32 s91, s55, 0
	s_mov_b32 m0, s65
	s_nop 0
	global_load_lds_dwordx4 v142, s[90:91]
	s_nop 0
	s_mov_b32 m0, s66
	s_nop 0
	global_load_lds_dwordx4 v144, s[90:91]
	s_waitcnt vmcnt(8)
	s_waitcnt lgkmcnt(0)
	s_barrier
	s_setprio 1
	v_mfma_scale_f32_16x16x128_f8f6f4 v[124:127], v[0:7], v[8:15], v[124:127], v150, v149 op_sel_hi:[0,0,0]
	v_mfma_scale_f32_16x16x128_f8f6f4 v[120:123], v[16:23], v[8:15], v[120:123], v150, v149 op_sel_hi:[0,0,0]
	v_mfma_scale_f32_16x16x128_f8f6f4 v[108:111], v[0:7], v[24:31], v[108:111], v150, v149 op_sel_hi:[0,0,0]
	v_mfma_scale_f32_16x16x128_f8f6f4 v[104:107], v[16:23], v[24:31], v[104:107], v150, v149 op_sel_hi:[0,0,0]
	v_mfma_scale_f32_16x16x128_f8f6f4 v[92:95], v[0:7], v[32:39], v[138:141], v150, v149 op_sel_hi:[0,0,0]
	v_mfma_scale_f32_16x16x128_f8f6f4 v[88:91], v[16:23], v[32:39], v[210:213], v150, v149 op_sel_hi:[0,0,0]
	v_mfma_scale_f32_16x16x128_f8f6f4 v[76:79], v[0:7], v[40:47], v[214:217], v150, v149 op_sel_hi:[0,0,0]
	v_mfma_scale_f32_16x16x128_f8f6f4 v[72:75], v[16:23], v[40:47], v[218:221], v150, v149 op_sel_hi:[0,0,0]
	s_setprio 0
	s_setprio 1
	v_mfma_scale_f32_16x16x128_f8f6f4 v[116:119], v[130:137], v[8:15], v[116:119], v150, v149 op_sel_hi:[0,0,0]
	v_mfma_scale_f32_16x16x128_f8f6f4 v[112:115], v[154:161], v[8:15], v[112:115], v150, v149 op_sel_hi:[0,0,0]
	v_mfma_scale_f32_16x16x128_f8f6f4 v[100:103], v[130:137], v[24:31], v[100:103], v150, v149 op_sel_hi:[0,0,0]
	v_mfma_scale_f32_16x16x128_f8f6f4 v[96:99], v[154:161], v[24:31], v[96:99], v150, v149 op_sel_hi:[0,0,0]
	v_mfma_scale_f32_16x16x128_f8f6f4 v[84:87], v[130:137], v[32:39], v[178:181], v150, v149 op_sel_hi:[0,0,0]
	v_mfma_scale_f32_16x16x128_f8f6f4 v[80:83], v[154:161], v[32:39], v[182:185], v150, v149 op_sel_hi:[0,0,0]
	v_mfma_scale_f32_16x16x128_f8f6f4 v[68:71], v[130:137], v[40:47], v[186:189], v150, v149 op_sel_hi:[0,0,0]
	v_mfma_scale_f32_16x16x128_f8f6f4 v[64:67], v[154:161], v[40:47], v[190:193], v150, v149 op_sel_hi:[0,0,0]
	s_setprio 0
	s_barrier
	ds_read_b128 v[32:35], v148 offset:49152
	ds_read_b128 v[36:39], v148 offset:49168
	ds_read_b128 v[162:165], v148 offset:51200
	ds_read_b128 v[166:169], v148 offset:51216
	ds_read_b128 v[170:173], v148 offset:53248
	ds_read_b128 v[174:177], v148 offset:53264
	ds_read_b128 v[178:181], v148 offset:55296
	ds_read_b128 v[182:185], v148 offset:55312
	s_add_u32 s90, s42, 0x80
	s_addc_u32 s91, s43, 0
	s_mov_b32 m0, s74
	s_nop 0
	global_load_lds_dwordx4 v143, s[90:91]
	s_add_u32 s42, s42, 0x40080
	s_mov_b32 m0, s75
	s_nop 0
	global_load_lds_dwordx4 v145, s[90:91]
	s_addc_u32 s43, s43, 0
	s_mov_b32 m0, s78
	s_nop 0
	global_load_lds_dwordx4 v143, s[42:43]
	s_nop 0
	s_mov_b32 m0, s79
	s_nop 0
	global_load_lds_dwordx4 v145, s[42:43]
	s_add_u32 s42, s54, 0x80
	s_addc_u32 s43, s55, 0
	s_mov_b32 m0, s76
	s_nop 0
	global_load_lds_dwordx4 v142, s[42:43]
	s_nop 0
	s_mov_b32 m0, s77
	s_nop 0
	global_load_lds_dwordx4 v144, s[42:43]
	s_waitcnt vmcnt(8)
	s_waitcnt lgkmcnt(0)
	s_barrier
	s_setprio 1
	v_mfma_scale_f32_16x16x128_f8f6f4 v[60:63], v[0:7], v[32:39], v[60:63], v150, v149 op_sel_hi:[0,0,0]
	v_mfma_scale_f32_16x16x128_f8f6f4 v[56:59], v[16:23], v[32:39], v[56:59], v150, v149 op_sel_hi:[0,0,0]
	v_mfma_scale_f32_16x16x128_f8f6f4 v[44:47], v[0:7], v[162:169], v[194:197], v150, v149 op_sel_hi:[0,0,0]
	v_mfma_scale_f32_16x16x128_f8f6f4 v[40:43], v[16:23], v[162:169], v[198:201], v150, v149 op_sel_hi:[0,0,0]
	v_mfma_scale_f32_16x16x128_f8f6f4 v[28:31], v[0:7], v[170:177], v[202:205], v150, v149 op_sel_hi:[0,0,0]
	v_mfma_scale_f32_16x16x128_f8f6f4 v[24:27], v[16:23], v[170:177], v[206:209], v150, v149 op_sel_hi:[0,0,0]
	v_mfma_scale_f32_16x16x128_f8f6f4 v[12:15], v[0:7], v[178:185], v[222:225], v150, v149 op_sel_hi:[0,0,0]
	v_mfma_scale_f32_16x16x128_f8f6f4 v[8:11], v[16:23], v[178:185], v[226:229], v150, v149 op_sel_hi:[0,0,0]
	s_setprio 0
	s_setprio 1
	v_mfma_scale_f32_16x16x128_f8f6f4 v[52:55], v[130:137], v[32:39], v[52:55], v150, v149 op_sel_hi:[0,0,0]
	v_mfma_scale_f32_16x16x128_f8f6f4 v[48:51], v[154:161], v[32:39], v[48:51], v150, v149 op_sel_hi:[0,0,0]
	v_mfma_scale_f32_16x16x128_f8f6f4 v[36:39], v[130:137], v[162:169], v[230:233], v150, v149 op_sel_hi:[0,0,0]
	v_mfma_scale_f32_16x16x128_f8f6f4 v[32:35], v[154:161], v[162:169], v[234:237], v150, v149 op_sel_hi:[0,0,0]
	v_mfma_scale_f32_16x16x128_f8f6f4 v[20:23], v[130:137], v[170:177], v[238:241], v150, v149 op_sel_hi:[0,0,0]
	v_mfma_scale_f32_16x16x128_f8f6f4 v[16:19], v[154:161], v[170:177], v[242:245], v150, v149 op_sel_hi:[0,0,0]
	v_mfma_scale_f32_16x16x128_f8f6f4 v[4:7], v[130:137], v[178:185], v[246:249], v150, v149 op_sel_hi:[0,0,0]
	v_mfma_scale_f32_16x16x128_f8f6f4 v[0:3], v[154:161], v[178:185], v[250:253], v150, v149 op_sel_hi:[0,0,0]
	s_setprio 0
	s_barrier
	s_add_i32 s23, s23, 2
	s_add_u32 s40, s40, 0x100
	s_addc_u32 s41, s41, 0
	s_cmp_gt_u32 s23, 13
	s_cbranch_scc0 .LBB4_1541
	s_and_b64 vcc, exec, s[10:11]
	s_cbranch_vccz .LBB4_1544
	s_barrier
